# v7: rewrote the int8 SwiGLU epilogues of P6 and P14 by hand (packed f32 mul/add, folded scale constants, in-place cvt), on top of v3
# speedup vs baseline: 1.0332x; 1.0174x over previous
; __device__ __forceinline__ unsigned cvt4_fp8(float a, float b, float c, float d) { int w = 0; w = __builtin_amdgcn_cvt_pk_fp8_f32(clamp448(a), clamp448(b), w, false); w = __builtin_amdgcn_cvt_pk_fp8_f32(clamp448(c), clamp448(d), w, true); return (unsigned)w; }
; __device__ __forceinline__ u32x4 pack8(const f32x4 a, const f32x4 b) { u32x4 w; w.x = cvt_pk_bf16(a[0], a[1]); w.y = cvt_pk_bf16(a[2], a[3]); w.z = cvt_pk_bf16(b[0], b[1]); w.w = cvt_pk_bf16(b[2], b[3]); return w; }
; __device__ __forceinline__ float sigmoidf_(float x) { return __builtin_amdgcn_rcpf(1.0f + __expf(-x)); }
; __device__ __forceinline__ float siluf_(float x) { return x * sigmoidf_(x); }
;     __device__ __forceinline__ void operator()(const AccT& acc, const Unit& u, int wr, int wc, int fr, int fq) const {
;     ...
;         f32x4 cg0 = *(const f32x4*)(cmax + nb) * (1.0f / 127.0f), cg1 = *(const f32x4*)(cmax + nb + 4) * (1.0f / 127.0f), cu0 = *(const f32x4*)(cmax + nb + 128) * (1.0f / 127.0f), cu1 = *(const f32x4*)(cmax + nb + 132) * (1.0f / 127.0f);
; #pragma unroll
;         for (int ai = 0; ai < 2; ++ai)
; #pragma unroll
;             for (int m = 0; m < 4; ++m) { const int row = row0 + ai * HALF + m * 16; const float rs = rsc[row]; f32x4 z0, z1;
;                 const i32x4v g0 = __builtin_bit_cast(i32x4v, acc[ai][0][m][0]), g1 = __builtin_bit_cast(i32x4v, acc[ai][0][m][1]), u0 = __builtin_bit_cast(i32x4v, acc[ai][1][m][0]), u1 = __builtin_bit_cast(i32x4v, acc[ai][1][m][1]);
; #pragma unroll
;                 for (int j = 0; j < 4; ++j) { z0[j] = siluf_((float)g0[j] * (rs * cg0[j])) * ((float)u0[j] * (rs * cu0[j])); z1[j] = siluf_((float)g1[j] * (rs * cg1[j])) * ((float)u1[j] * (rs * cu1[j])); }
;                 if (sout8 > 0.f) { u32x2 w; w.x = cvt4_fp8(z0[0] * sout8, z0[1] * sout8, z0[2] * sout8, z0[3] * sout8); w.y = cvt4_fp8(z1[0] * sout8, z1[1] * sout8, z1[2] * sout8, z1[3] * sout8); *(u32x2*)((unsigned char*)O + (size_t)row * ldo + cb) = w; }
;                 else *(u32x4*)(O + (size_t)row * ldo + cb) = pack8(z0, z1);
;                 __builtin_amdgcn_sched_barrier(0); }
.LBB0_1420:
	v_lshl_or_b32 v130, s63, 8, v177
	v_ashrrev_i32_e32 v131, 31, v130
	v_lshl_add_u64 v[130:131], v[130:131], 2, s[16:17]
	v_add_u32_e32 v132, s62, v175
	global_load_dwordx4 v[136:139], v[130:131], off offset:512
	global_load_dwordx4 v[140:143], v[130:131], off
	global_load_dwordx4 v[144:147], v[130:131], off offset:528
	global_load_dwordx4 v[148:151], v[130:131], off offset:16
	v_ashrrev_i32_e32 v133, 31, v132
	v_lshl_add_u64 v[134:135], v[132:133], 2, s[14:15]
	global_load_dword v152, v[134:135], off
	global_load_dword v211, v[134:135], off offset:64
	global_load_dword v212, v[134:135], off offset:128
	global_load_dword v213, v[134:135], off offset:192
	global_load_dword v214, v[134:135], off offset:512
	global_load_dword v215, v[134:135], off offset:576
	global_load_dword v216, v[134:135], off offset:640
	global_load_dword v217, v[134:135], off offset:704
	s_nop 0
	s_nop 0
	s_nop 0
	s_nop 0
	s_nop 0
	s_nop 0
	s_nop 0
	s_nop 0
	s_nop 0
	s_nop 0
	s_nop 0
	s_nop 0
	s_nop 0
	s_nop 0
	s_nop 0
	s_nop 0
	v_lshl_or_b32 v130, s63, 7, v177
	v_ashrrev_i32_e32 v131, 31, v130
	s_waitcnt vmcnt(0)
	s_mov_b32 s98, 0xbc3a1e78
	s_mov_b32 s100, 0x39820610
	v_pk_mul_f32 v[132:133], v[140:141], s[98:99] op_sel_hi:[1,0]
	v_pk_mul_f32 v[134:135], v[142:143], s[98:99] op_sel_hi:[1,0]
	v_pk_mul_f32 v[154:155], v[148:149], s[98:99] op_sel_hi:[1,0]
	v_pk_mul_f32 v[156:157], v[150:151], s[98:99] op_sel_hi:[1,0]
	v_pk_mul_f32 v[158:159], v[140:141], v[136:137]
	v_pk_mul_f32 v[160:161], v[142:143], v[138:139]
	v_pk_mul_f32 v[186:187], v[148:149], v[144:145]
	v_pk_mul_f32 v[188:189], v[150:151], v[146:147]
	v_add_u32_e32 v207, s62, v175
	v_mov_b64_e32 v[200:201], s[6:7]
	v_pk_mul_f32 v[158:159], v[158:159], s[100:101] op_sel_hi:[1,0]
	v_pk_mul_f32 v[160:161], v[160:161], s[100:101] op_sel_hi:[1,0]
	v_pk_mul_f32 v[186:187], v[186:187], s[100:101] op_sel_hi:[1,0]
	v_pk_mul_f32 v[188:189], v[188:189], s[100:101] op_sel_hi:[1,0]
	v_mad_i64_i32 v[198:199], s[34:35], v207, s59, v[200:201]
	v_lshl_add_u64 v[198:199], v[198:199], 0, v[130:131]
	s_mov_b32 s101, 0
	v_cvt_f32_i32_e32 v126, v126
	v_cvt_f32_i32_e32 v127, v127
	v_cvt_f32_i32_e32 v128, v128
	v_cvt_f32_i32_e32 v129, v129
	v_cvt_f32_i32_e32 v122, v122
	v_cvt_f32_i32_e32 v123, v123
	v_cvt_f32_i32_e32 v124, v124
	v_cvt_f32_i32_e32 v125, v125
	v_cvt_f32_i32_e32 v118, v118
	v_cvt_f32_i32_e32 v119, v119
	v_cvt_f32_i32_e32 v120, v120
	v_cvt_f32_i32_e32 v121, v121
	v_cvt_f32_i32_e32 v114, v114
	v_cvt_f32_i32_e32 v115, v115
	v_cvt_f32_i32_e32 v116, v116
	v_cvt_f32_i32_e32 v117, v117
	v_mul_f32_e32 v206, v152, v152
	v_pk_mul_f32 v[136:137], v[152:153], v[132:133] op_sel_hi:[0,1]
	v_pk_mul_f32 v[138:139], v[152:153], v[134:135] op_sel_hi:[0,1]
	v_pk_mul_f32 v[140:141], v[152:153], v[154:155] op_sel_hi:[0,1]
	v_pk_mul_f32 v[142:143], v[152:153], v[156:157] op_sel_hi:[0,1]
	v_pk_mul_f32 v[190:191], v[126:127], v[136:137]
	v_pk_mul_f32 v[192:193], v[128:129], v[138:139]
	v_pk_mul_f32 v[194:195], v[122:123], v[140:141]
	v_pk_mul_f32 v[196:197], v[124:125], v[142:143]
	v_exp_f32_e32 v190, v190
	v_exp_f32_e32 v191, v191
	v_exp_f32_e32 v192, v192
	v_exp_f32_e32 v193, v193
	v_exp_f32_e32 v194, v194
	v_exp_f32_e32 v195, v195
	v_exp_f32_e32 v196, v196
	v_exp_f32_e32 v197, v197
	v_pk_mul_f32 v[118:119], v[126:127], v[118:119]
	v_pk_mul_f32 v[120:121], v[128:129], v[120:121]
	v_pk_mul_f32 v[114:115], v[122:123], v[114:115]
	v_pk_mul_f32 v[116:117], v[124:125], v[116:117]
	v_pk_mul_f32 v[144:145], v[206:207], v[158:159] op_sel_hi:[0,1]
	v_pk_mul_f32 v[146:147], v[206:207], v[160:161] op_sel_hi:[0,1]
	v_pk_mul_f32 v[148:149], v[206:207], v[186:187] op_sel_hi:[0,1]
	v_pk_mul_f32 v[150:151], v[206:207], v[188:189] op_sel_hi:[0,1]
	v_pk_add_f32 v[190:191], v[190:191], 1.0 op_sel_hi:[1,0]
	v_pk_add_f32 v[192:193], v[192:193], 1.0 op_sel_hi:[1,0]
	v_pk_add_f32 v[194:195], v[194:195], 1.0 op_sel_hi:[1,0]
	v_pk_add_f32 v[196:197], v[196:197], 1.0 op_sel_hi:[1,0]
	v_rcp_f32_e32 v190, v190
	v_rcp_f32_e32 v191, v191
	v_rcp_f32_e32 v192, v192
	v_rcp_f32_e32 v193, v193
	v_rcp_f32_e32 v194, v194
	v_rcp_f32_e32 v195, v195
	v_rcp_f32_e32 v196, v196
	v_rcp_f32_e32 v197, v197
	v_pk_mul_f32 v[118:119], v[118:119], v[144:145]
	v_pk_mul_f32 v[120:121], v[120:121], v[146:147]
	v_pk_mul_f32 v[114:115], v[114:115], v[148:149]
	v_pk_mul_f32 v[116:117], v[116:117], v[150:151]
	s_mov_b32 s100, 0x0
	v_pk_mul_f32 v[118:119], v[118:119], v[190:191]
	v_pk_mul_f32 v[120:121], v[120:121], v[192:193]
	v_pk_mul_f32 v[114:115], v[114:115], v[194:195]
	v_pk_mul_f32 v[116:117], v[116:117], v[196:197]
	v_med3_f32 v118, v118, s58, v181
	v_med3_f32 v119, v119, s58, v181
	v_med3_f32 v120, v120, s58, v181
	v_med3_f32 v121, v121, s58, v181
	v_med3_f32 v114, v114, s58, v181
	v_med3_f32 v115, v115, s58, v181
	v_med3_f32 v116, v116, s58, v181
	v_med3_f32 v117, v117, s58, v181
	v_cvt_pk_fp8_f32 v204, v118, v119
	v_cvt_pk_fp8_f32 v205, v114, v115
	v_lshl_add_u64 v[202:203], v[198:199], 0, s[100:101]
	v_cvt_pk_fp8_f32 v204, v120, v121 op_sel:[0,0,1]
	v_cvt_pk_fp8_f32 v205, v116, v117 op_sel:[0,0,1]
	s_nop 0
	global_store_dwordx2 v[202:203], v[204:205], off
	v_cvt_f32_i32_e32 v110, v110
	v_cvt_f32_i32_e32 v111, v111
	v_cvt_f32_i32_e32 v112, v112
	v_cvt_f32_i32_e32 v113, v113
	v_cvt_f32_i32_e32 v106, v106
	v_cvt_f32_i32_e32 v107, v107
	v_cvt_f32_i32_e32 v108, v108
	v_cvt_f32_i32_e32 v109, v109
	v_cvt_f32_i32_e32 v102, v102
	v_cvt_f32_i32_e32 v103, v103
	v_cvt_f32_i32_e32 v104, v104
	v_cvt_f32_i32_e32 v105, v105
	v_cvt_f32_i32_e32 v98, v98
	v_cvt_f32_i32_e32 v99, v99
	v_cvt_f32_i32_e32 v100, v100
	v_cvt_f32_i32_e32 v101, v101
	v_mul_f32_e32 v206, v211, v211
; __device__ __forceinline__ unsigned cvt4_fp8(float a, float b, float c, float d) { int w = 0; w = __builtin_amdgcn_cvt_pk_fp8_f32(clamp448(a), clamp448(b), w, false); w = __builtin_amdgcn_cvt_pk_fp8_f32(clamp448(c), clamp448(d), w, true); return (unsigned)w; }
; __device__ __forceinline__ float siluf_(float x) { return x * sigmoidf_(x); }
; __device__ __forceinline__ u32x4 pack8(const f32x4 a, const f32x4 b) { u32x4 w; w.x = cvt_pk_bf16(a[0], a[1]); w.y = cvt_pk_bf16(a[2], a[3]); w.z = cvt_pk_bf16(b[0], b[1]); w.w = cvt_pk_bf16(b[2], b[3]); return w; }
;     __device__ __forceinline__ void operator()(const AccT& acc, const Unit& u, int wr, int wc, int fr, int fq) const {
;     ...
;             for (int m = 0; m < 4; ++m) { const int row = row0 + ai * HALF + m * 16; const float rs = rsc[row]; f32x4 z0, z1;
;                 const i32x4v g0 = __builtin_bit_cast(i32x4v, acc[ai][0][m][0]), g1 = __builtin_bit_cast(i32x4v, acc[ai][0][m][1]), u0 = __builtin_bit_cast(i32x4v, acc[ai][1][m][0]), u1 = __builtin_bit_cast(i32x4v, acc[ai][1][m][1]);
; #pragma unroll
;                 for (int j = 0; j < 4; ++j) { z0[j] = siluf_((float)g0[j] * (rs * cg0[j])) * ((float)u0[j] * (rs * cu0[j])); z1[j] = siluf_((float)g1[j] * (rs * cg1[j])) * ((float)u1[j] * (rs * cu1[j])); }
;                 if (sout8 > 0.f) { u32x2 w; w.x = cvt4_fp8(z0[0] * sout8, z0[1] * sout8, z0[2] * sout8, z0[3] * sout8); w.y = cvt4_fp8(z1[0] * sout8, z1[1] * sout8, z1[2] * sout8, z1[3] * sout8); *(u32x2*)((unsigned char*)O + (size_t)row * ldo + cb) = w; }
;                 else *(u32x4*)(O + (size_t)row * ldo + cb) = pack8(z0, z1);
;                 __builtin_amdgcn_sched_barrier(0); }
	v_pk_mul_f32 v[136:137], v[210:211], v[132:133] op_sel:[1,0] op_sel_hi:[1,1]
	v_pk_mul_f32 v[138:139], v[210:211], v[134:135] op_sel:[1,0] op_sel_hi:[1,1]
	v_pk_mul_f32 v[140:141], v[210:211], v[154:155] op_sel:[1,0] op_sel_hi:[1,1]
	v_pk_mul_f32 v[142:143], v[210:211], v[156:157] op_sel:[1,0] op_sel_hi:[1,1]
	v_pk_mul_f32 v[190:191], v[110:111], v[136:137]
	v_pk_mul_f32 v[192:193], v[112:113], v[138:139]
	v_pk_mul_f32 v[194:195], v[106:107], v[140:141]
	v_pk_mul_f32 v[196:197], v[108:109], v[142:143]
	v_exp_f32_e32 v190, v190
	v_exp_f32_e32 v191, v191
	v_exp_f32_e32 v192, v192
	v_exp_f32_e32 v193, v193
	v_exp_f32_e32 v194, v194
	v_exp_f32_e32 v195, v195
	v_exp_f32_e32 v196, v196
	v_exp_f32_e32 v197, v197
	v_pk_mul_f32 v[102:103], v[110:111], v[102:103]
	v_pk_mul_f32 v[104:105], v[112:113], v[104:105]
	v_pk_mul_f32 v[98:99], v[106:107], v[98:99]
	v_pk_mul_f32 v[100:101], v[108:109], v[100:101]
	v_pk_mul_f32 v[144:145], v[206:207], v[158:159] op_sel_hi:[0,1]
	v_pk_mul_f32 v[146:147], v[206:207], v[160:161] op_sel_hi:[0,1]
	v_pk_mul_f32 v[148:149], v[206:207], v[186:187] op_sel_hi:[0,1]
	v_pk_mul_f32 v[150:151], v[206:207], v[188:189] op_sel_hi:[0,1]
	v_pk_add_f32 v[190:191], v[190:191], 1.0 op_sel_hi:[1,0]
	v_pk_add_f32 v[192:193], v[192:193], 1.0 op_sel_hi:[1,0]
	v_pk_add_f32 v[194:195], v[194:195], 1.0 op_sel_hi:[1,0]
	v_pk_add_f32 v[196:197], v[196:197], 1.0 op_sel_hi:[1,0]
	v_rcp_f32_e32 v190, v190
	v_rcp_f32_e32 v191, v191
	v_rcp_f32_e32 v192, v192
	v_rcp_f32_e32 v193, v193
	v_rcp_f32_e32 v194, v194
	v_rcp_f32_e32 v195, v195
	v_rcp_f32_e32 v196, v196
	v_rcp_f32_e32 v197, v197
	v_pk_mul_f32 v[102:103], v[102:103], v[144:145]
	v_pk_mul_f32 v[104:105], v[104:105], v[146:147]
	v_pk_mul_f32 v[98:99], v[98:99], v[148:149]
	v_pk_mul_f32 v[100:101], v[100:101], v[150:151]
	s_mov_b32 s100, 0x16000
	v_pk_mul_f32 v[102:103], v[102:103], v[190:191]
	v_pk_mul_f32 v[104:105], v[104:105], v[192:193]
	v_pk_mul_f32 v[98:99], v[98:99], v[194:195]
	v_pk_mul_f32 v[100:101], v[100:101], v[196:197]
	v_med3_f32 v102, v102, s58, v181
	v_med3_f32 v103, v103, s58, v181
	v_med3_f32 v104, v104, s58, v181
	v_med3_f32 v105, v105, s58, v181
	v_med3_f32 v98, v98, s58, v181
	v_med3_f32 v99, v99, s58, v181
	v_med3_f32 v100, v100, s58, v181
	v_med3_f32 v101, v101, s58, v181
	v_cvt_pk_fp8_f32 v204, v102, v103
	v_cvt_pk_fp8_f32 v205, v98, v99
	v_lshl_add_u64 v[202:203], v[198:199], 0, s[100:101]
	v_cvt_pk_fp8_f32 v204, v104, v105 op_sel:[0,0,1]
	v_cvt_pk_fp8_f32 v205, v100, v101 op_sel:[0,0,1]
	s_nop 0
	global_store_dwordx2 v[202:203], v[204:205], off
	v_cvt_f32_i32_e32 v94, v94
	v_cvt_f32_i32_e32 v95, v95
	v_cvt_f32_i32_e32 v96, v96
	v_cvt_f32_i32_e32 v97, v97
	v_cvt_f32_i32_e32 v90, v90
	v_cvt_f32_i32_e32 v91, v91
	v_cvt_f32_i32_e32 v92, v92
	v_cvt_f32_i32_e32 v93, v93
	v_cvt_f32_i32_e32 v86, v86
	v_cvt_f32_i32_e32 v87, v87
	v_cvt_f32_i32_e32 v88, v88
	v_cvt_f32_i32_e32 v89, v89
	v_cvt_f32_i32_e32 v82, v82
	v_cvt_f32_i32_e32 v83, v83
	v_cvt_f32_i32_e32 v84, v84
	v_cvt_f32_i32_e32 v85, v85
	v_mul_f32_e32 v206, v212, v212
	v_pk_mul_f32 v[136:137], v[212:213], v[132:133] op_sel_hi:[0,1]
	v_pk_mul_f32 v[138:139], v[212:213], v[134:135] op_sel_hi:[0,1]
	v_pk_mul_f32 v[140:141], v[212:213], v[154:155] op_sel_hi:[0,1]
	v_pk_mul_f32 v[142:143], v[212:213], v[156:157] op_sel_hi:[0,1]
	v_pk_mul_f32 v[190:191], v[94:95], v[136:137]
	v_pk_mul_f32 v[192:193], v[96:97], v[138:139]
	v_pk_mul_f32 v[194:195], v[90:91], v[140:141]
	v_pk_mul_f32 v[196:197], v[92:93], v[142:143]
	v_exp_f32_e32 v190, v190
	v_exp_f32_e32 v191, v191
	v_exp_f32_e32 v192, v192
	v_exp_f32_e32 v193, v193
	v_exp_f32_e32 v194, v194
	v_exp_f32_e32 v195, v195
	v_exp_f32_e32 v196, v196
	v_exp_f32_e32 v197, v197
	v_pk_mul_f32 v[86:87], v[94:95], v[86:87]
	v_pk_mul_f32 v[88:89], v[96:97], v[88:89]
	v_pk_mul_f32 v[82:83], v[90:91], v[82:83]
	v_pk_mul_f32 v[84:85], v[92:93], v[84:85]
	v_pk_mul_f32 v[144:145], v[206:207], v[158:159] op_sel_hi:[0,1]
	v_pk_mul_f32 v[146:147], v[206:207], v[160:161] op_sel_hi:[0,1]
	v_pk_mul_f32 v[148:149], v[206:207], v[186:187] op_sel_hi:[0,1]
	v_pk_mul_f32 v[150:151], v[206:207], v[188:189] op_sel_hi:[0,1]
	v_pk_add_f32 v[190:191], v[190:191], 1.0 op_sel_hi:[1,0]
	v_pk_add_f32 v[192:193], v[192:193], 1.0 op_sel_hi:[1,0]
	v_pk_add_f32 v[194:195], v[194:195], 1.0 op_sel_hi:[1,0]
	v_pk_add_f32 v[196:197], v[196:197], 1.0 op_sel_hi:[1,0]
	v_rcp_f32_e32 v190, v190
	v_rcp_f32_e32 v191, v191
	v_rcp_f32_e32 v192, v192
	v_rcp_f32_e32 v193, v193
	v_rcp_f32_e32 v194, v194
	v_rcp_f32_e32 v195, v195
	v_rcp_f32_e32 v196, v196
	v_rcp_f32_e32 v197, v197
	v_pk_mul_f32 v[86:87], v[86:87], v[144:145]
	v_pk_mul_f32 v[88:89], v[88:89], v[146:147]
	v_pk_mul_f32 v[82:83], v[82:83], v[148:149]
	v_pk_mul_f32 v[84:85], v[84:85], v[150:151]
	s_mov_b32 s100, 0x2c000
	v_pk_mul_f32 v[86:87], v[86:87], v[190:191]
	v_pk_mul_f32 v[88:89], v[88:89], v[192:193]
	v_pk_mul_f32 v[82:83], v[82:83], v[194:195]
	v_pk_mul_f32 v[84:85], v[84:85], v[196:197]
	v_med3_f32 v86, v86, s58, v181
	v_med3_f32 v87, v87, s58, v181
	v_med3_f32 v88, v88, s58, v181
	v_med3_f32 v89, v89, s58, v181
	v_med3_f32 v82, v82, s58, v181
	v_med3_f32 v83, v83, s58, v181
	v_med3_f32 v84, v84, s58, v181
	v_med3_f32 v85, v85, s58, v181
	v_cvt_pk_fp8_f32 v204, v86, v87
	v_cvt_pk_fp8_f32 v205, v82, v83
	v_lshl_add_u64 v[202:203], v[198:199], 0, s[100:101]
	v_cvt_pk_fp8_f32 v204, v88, v89 op_sel:[0,0,1]
	v_cvt_pk_fp8_f32 v205, v84, v85 op_sel:[0,0,1]
	s_nop 0
	global_store_dwordx2 v[202:203], v[204:205], off
	v_cvt_f32_i32_e32 v78, v78
	v_cvt_f32_i32_e32 v79, v79
	v_cvt_f32_i32_e32 v80, v80
	v_cvt_f32_i32_e32 v81, v81
	v_cvt_f32_i32_e32 v74, v74
; __device__ __forceinline__ unsigned cvt4_fp8(float a, float b, float c, float d) { int w = 0; w = __builtin_amdgcn_cvt_pk_fp8_f32(clamp448(a), clamp448(b), w, false); w = __builtin_amdgcn_cvt_pk_fp8_f32(clamp448(c), clamp448(d), w, true); return (unsigned)w; }
; __device__ __forceinline__ float siluf_(float x) { return x * sigmoidf_(x); }
; __device__ __forceinline__ u32x4 pack8(const f32x4 a, const f32x4 b) { u32x4 w; w.x = cvt_pk_bf16(a[0], a[1]); w.y = cvt_pk_bf16(a[2], a[3]); w.z = cvt_pk_bf16(b[0], b[1]); w.w = cvt_pk_bf16(b[2], b[3]); return w; }
;     __device__ __forceinline__ void operator()(const AccT& acc, const Unit& u, int wr, int wc, int fr, int fq) const {
;     ...
;             for (int m = 0; m < 4; ++m) { const int row = row0 + ai * HALF + m * 16; const float rs = rsc[row]; f32x4 z0, z1;
;                 const i32x4v g0 = __builtin_bit_cast(i32x4v, acc[ai][0][m][0]), g1 = __builtin_bit_cast(i32x4v, acc[ai][0][m][1]), u0 = __builtin_bit_cast(i32x4v, acc[ai][1][m][0]), u1 = __builtin_bit_cast(i32x4v, acc[ai][1][m][1]);
; #pragma unroll
;                 for (int j = 0; j < 4; ++j) { z0[j] = siluf_((float)g0[j] * (rs * cg0[j])) * ((float)u0[j] * (rs * cu0[j])); z1[j] = siluf_((float)g1[j] * (rs * cg1[j])) * ((float)u1[j] * (rs * cu1[j])); }
;                 if (sout8 > 0.f) { u32x2 w; w.x = cvt4_fp8(z0[0] * sout8, z0[1] * sout8, z0[2] * sout8, z0[3] * sout8); w.y = cvt4_fp8(z1[0] * sout8, z1[1] * sout8, z1[2] * sout8, z1[3] * sout8); *(u32x2*)((unsigned char*)O + (size_t)row * ldo + cb) = w; }
;                 else *(u32x4*)(O + (size_t)row * ldo + cb) = pack8(z0, z1);
;                 __builtin_amdgcn_sched_barrier(0); }
	v_cvt_f32_i32_e32 v75, v75
	v_cvt_f32_i32_e32 v76, v76
	v_cvt_f32_i32_e32 v77, v77
	v_cvt_f32_i32_e32 v70, v70
	v_cvt_f32_i32_e32 v71, v71
	v_cvt_f32_i32_e32 v72, v72
	v_cvt_f32_i32_e32 v73, v73
	v_cvt_f32_i32_e32 v66, v66
	v_cvt_f32_i32_e32 v67, v67
	v_cvt_f32_i32_e32 v68, v68
	v_cvt_f32_i32_e32 v69, v69
	v_mul_f32_e32 v206, v213, v213
	v_pk_mul_f32 v[136:137], v[212:213], v[132:133] op_sel:[1,0] op_sel_hi:[1,1]
	v_pk_mul_f32 v[138:139], v[212:213], v[134:135] op_sel:[1,0] op_sel_hi:[1,1]
	v_pk_mul_f32 v[140:141], v[212:213], v[154:155] op_sel:[1,0] op_sel_hi:[1,1]
	v_pk_mul_f32 v[142:143], v[212:213], v[156:157] op_sel:[1,0] op_sel_hi:[1,1]
	v_pk_mul_f32 v[190:191], v[78:79], v[136:137]
	v_pk_mul_f32 v[192:193], v[80:81], v[138:139]
	v_pk_mul_f32 v[194:195], v[74:75], v[140:141]
	v_pk_mul_f32 v[196:197], v[76:77], v[142:143]
	v_exp_f32_e32 v190, v190
	v_exp_f32_e32 v191, v191
	v_exp_f32_e32 v192, v192
	v_exp_f32_e32 v193, v193
	v_exp_f32_e32 v194, v194
	v_exp_f32_e32 v195, v195
	v_exp_f32_e32 v196, v196
	v_exp_f32_e32 v197, v197
	v_pk_mul_f32 v[70:71], v[78:79], v[70:71]
	v_pk_mul_f32 v[72:73], v[80:81], v[72:73]
	v_pk_mul_f32 v[66:67], v[74:75], v[66:67]
	v_pk_mul_f32 v[68:69], v[76:77], v[68:69]
	v_pk_mul_f32 v[144:145], v[206:207], v[158:159] op_sel_hi:[0,1]
	v_pk_mul_f32 v[146:147], v[206:207], v[160:161] op_sel_hi:[0,1]
	v_pk_mul_f32 v[148:149], v[206:207], v[186:187] op_sel_hi:[0,1]
	v_pk_mul_f32 v[150:151], v[206:207], v[188:189] op_sel_hi:[0,1]
	v_pk_add_f32 v[190:191], v[190:191], 1.0 op_sel_hi:[1,0]
	v_pk_add_f32 v[192:193], v[192:193], 1.0 op_sel_hi:[1,0]
	v_pk_add_f32 v[194:195], v[194:195], 1.0 op_sel_hi:[1,0]
	v_pk_add_f32 v[196:197], v[196:197], 1.0 op_sel_hi:[1,0]
	v_rcp_f32_e32 v190, v190
	v_rcp_f32_e32 v191, v191
	v_rcp_f32_e32 v192, v192
	v_rcp_f32_e32 v193, v193
	v_rcp_f32_e32 v194, v194
	v_rcp_f32_e32 v195, v195
	v_rcp_f32_e32 v196, v196
	v_rcp_f32_e32 v197, v197
	v_pk_mul_f32 v[70:71], v[70:71], v[144:145]
	v_pk_mul_f32 v[72:73], v[72:73], v[146:147]
	v_pk_mul_f32 v[66:67], v[66:67], v[148:149]
	v_pk_mul_f32 v[68:69], v[68:69], v[150:151]
	s_mov_b32 s100, 0x42000
	v_pk_mul_f32 v[70:71], v[70:71], v[190:191]
	v_pk_mul_f32 v[72:73], v[72:73], v[192:193]
	v_pk_mul_f32 v[66:67], v[66:67], v[194:195]
	v_pk_mul_f32 v[68:69], v[68:69], v[196:197]
	v_med3_f32 v70, v70, s58, v181
	v_med3_f32 v71, v71, s58, v181
	v_med3_f32 v72, v72, s58, v181
	v_med3_f32 v73, v73, s58, v181
	v_med3_f32 v66, v66, s58, v181
	v_med3_f32 v67, v67, s58, v181
	v_med3_f32 v68, v68, s58, v181
	v_med3_f32 v69, v69, s58, v181
	v_cvt_pk_fp8_f32 v204, v70, v71
	v_cvt_pk_fp8_f32 v205, v66, v67
	v_lshl_add_u64 v[202:203], v[198:199], 0, s[100:101]
	v_cvt_pk_fp8_f32 v204, v72, v73 op_sel:[0,0,1]
	v_cvt_pk_fp8_f32 v205, v68, v69 op_sel:[0,0,1]
	s_nop 0
	global_store_dwordx2 v[202:203], v[204:205], off
	v_cvt_f32_i32_e32 v62, v62
	v_cvt_f32_i32_e32 v63, v63
	v_cvt_f32_i32_e32 v64, v64
	v_cvt_f32_i32_e32 v65, v65
	v_cvt_f32_i32_e32 v58, v58
	v_cvt_f32_i32_e32 v59, v59
	v_cvt_f32_i32_e32 v60, v60
	v_cvt_f32_i32_e32 v61, v61
	v_cvt_f32_i32_e32 v54, v54
	v_cvt_f32_i32_e32 v55, v55
	v_cvt_f32_i32_e32 v56, v56
	v_cvt_f32_i32_e32 v57, v57
	v_cvt_f32_i32_e32 v50, v50
	v_cvt_f32_i32_e32 v51, v51
	v_cvt_f32_i32_e32 v52, v52
	v_cvt_f32_i32_e32 v53, v53
	v_mul_f32_e32 v206, v214, v214
	v_pk_mul_f32 v[136:137], v[214:215], v[132:133] op_sel_hi:[0,1]
	v_pk_mul_f32 v[138:139], v[214:215], v[134:135] op_sel_hi:[0,1]
	v_pk_mul_f32 v[140:141], v[214:215], v[154:155] op_sel_hi:[0,1]
	v_pk_mul_f32 v[142:143], v[214:215], v[156:157] op_sel_hi:[0,1]
	v_pk_mul_f32 v[190:191], v[62:63], v[136:137]
	v_pk_mul_f32 v[192:193], v[64:65], v[138:139]
	v_pk_mul_f32 v[194:195], v[58:59], v[140:141]
	v_pk_mul_f32 v[196:197], v[60:61], v[142:143]
	v_exp_f32_e32 v190, v190
	v_exp_f32_e32 v191, v191
	v_exp_f32_e32 v192, v192
	v_exp_f32_e32 v193, v193
	v_exp_f32_e32 v194, v194
	v_exp_f32_e32 v195, v195
	v_exp_f32_e32 v196, v196
	v_exp_f32_e32 v197, v197
	v_pk_mul_f32 v[54:55], v[62:63], v[54:55]
	v_pk_mul_f32 v[56:57], v[64:65], v[56:57]
	v_pk_mul_f32 v[50:51], v[58:59], v[50:51]
	v_pk_mul_f32 v[52:53], v[60:61], v[52:53]
	v_pk_mul_f32 v[144:145], v[206:207], v[158:159] op_sel_hi:[0,1]
	v_pk_mul_f32 v[146:147], v[206:207], v[160:161] op_sel_hi:[0,1]
	v_pk_mul_f32 v[148:149], v[206:207], v[186:187] op_sel_hi:[0,1]
	v_pk_mul_f32 v[150:151], v[206:207], v[188:189] op_sel_hi:[0,1]
	v_pk_add_f32 v[190:191], v[190:191], 1.0 op_sel_hi:[1,0]
	v_pk_add_f32 v[192:193], v[192:193], 1.0 op_sel_hi:[1,0]
	v_pk_add_f32 v[194:195], v[194:195], 1.0 op_sel_hi:[1,0]
	v_pk_add_f32 v[196:197], v[196:197], 1.0 op_sel_hi:[1,0]
	v_rcp_f32_e32 v190, v190
	v_rcp_f32_e32 v191, v191
	v_rcp_f32_e32 v192, v192
	v_rcp_f32_e32 v193, v193
	v_rcp_f32_e32 v194, v194
	v_rcp_f32_e32 v195, v195
	v_rcp_f32_e32 v196, v196
	v_rcp_f32_e32 v197, v197
	v_pk_mul_f32 v[54:55], v[54:55], v[144:145]
	v_pk_mul_f32 v[56:57], v[56:57], v[146:147]
	v_pk_mul_f32 v[50:51], v[50:51], v[148:149]
	v_pk_mul_f32 v[52:53], v[52:53], v[150:151]
	s_mov_b32 s100, 0xb0000
	v_pk_mul_f32 v[54:55], v[54:55], v[190:191]
	v_pk_mul_f32 v[56:57], v[56:57], v[192:193]
	v_pk_mul_f32 v[50:51], v[50:51], v[194:195]
	v_pk_mul_f32 v[52:53], v[52:53], v[196:197]
	v_med3_f32 v54, v54, s58, v181
	v_med3_f32 v55, v55, s58, v181
	v_med3_f32 v56, v56, s58, v181
	v_med3_f32 v57, v57, s58, v181
	v_med3_f32 v50, v50, s58, v181
	v_med3_f32 v51, v51, s58, v181
	v_med3_f32 v52, v52, s58, v181
	v_med3_f32 v53, v53, s58, v181
	v_cvt_pk_fp8_f32 v204, v54, v55
	v_cvt_pk_fp8_f32 v205, v50, v51
	v_lshl_add_u64 v[202:203], v[198:199], 0, s[100:101]
	v_cvt_pk_fp8_f32 v204, v56, v57 op_sel:[0,0,1]
; __device__ __forceinline__ unsigned cvt4_fp8(float a, float b, float c, float d) { int w = 0; w = __builtin_amdgcn_cvt_pk_fp8_f32(clamp448(a), clamp448(b), w, false); w = __builtin_amdgcn_cvt_pk_fp8_f32(clamp448(c), clamp448(d), w, true); return (unsigned)w; }
; __device__ __forceinline__ float siluf_(float x) { return x * sigmoidf_(x); }
; __device__ __forceinline__ u32x4 pack8(const f32x4 a, const f32x4 b) { u32x4 w; w.x = cvt_pk_bf16(a[0], a[1]); w.y = cvt_pk_bf16(a[2], a[3]); w.z = cvt_pk_bf16(b[0], b[1]); w.w = cvt_pk_bf16(b[2], b[3]); return w; }
;     __device__ __forceinline__ void operator()(const AccT& acc, const Unit& u, int wr, int wc, int fr, int fq) const {
;     ...
;             for (int m = 0; m < 4; ++m) { const int row = row0 + ai * HALF + m * 16; const float rs = rsc[row]; f32x4 z0, z1;
;                 const i32x4v g0 = __builtin_bit_cast(i32x4v, acc[ai][0][m][0]), g1 = __builtin_bit_cast(i32x4v, acc[ai][0][m][1]), u0 = __builtin_bit_cast(i32x4v, acc[ai][1][m][0]), u1 = __builtin_bit_cast(i32x4v, acc[ai][1][m][1]);
; #pragma unroll
;                 for (int j = 0; j < 4; ++j) { z0[j] = siluf_((float)g0[j] * (rs * cg0[j])) * ((float)u0[j] * (rs * cu0[j])); z1[j] = siluf_((float)g1[j] * (rs * cg1[j])) * ((float)u1[j] * (rs * cu1[j])); }
;                 if (sout8 > 0.f) { u32x2 w; w.x = cvt4_fp8(z0[0] * sout8, z0[1] * sout8, z0[2] * sout8, z0[3] * sout8); w.y = cvt4_fp8(z1[0] * sout8, z1[1] * sout8, z1[2] * sout8, z1[3] * sout8); *(u32x2*)((unsigned char*)O + (size_t)row * ldo + cb) = w; }
;                 else *(u32x4*)(O + (size_t)row * ldo + cb) = pack8(z0, z1);
;                 __builtin_amdgcn_sched_barrier(0); }
	v_cvt_pk_fp8_f32 v205, v52, v53 op_sel:[0,0,1]
	s_nop 0
	global_store_dwordx2 v[202:203], v[204:205], off
	v_cvt_f32_i32_e32 v46, v46
	v_cvt_f32_i32_e32 v47, v47
	v_cvt_f32_i32_e32 v48, v48
	v_cvt_f32_i32_e32 v49, v49
	v_cvt_f32_i32_e32 v42, v42
	v_cvt_f32_i32_e32 v43, v43
	v_cvt_f32_i32_e32 v44, v44
	v_cvt_f32_i32_e32 v45, v45
	v_cvt_f32_i32_e32 v38, v38
	v_cvt_f32_i32_e32 v39, v39
	v_cvt_f32_i32_e32 v40, v40
	v_cvt_f32_i32_e32 v41, v41
	v_cvt_f32_i32_e32 v34, v34
	v_cvt_f32_i32_e32 v35, v35
	v_cvt_f32_i32_e32 v36, v36
	v_cvt_f32_i32_e32 v37, v37
	v_mul_f32_e32 v206, v215, v215
	v_pk_mul_f32 v[136:137], v[214:215], v[132:133] op_sel:[1,0] op_sel_hi:[1,1]
	v_pk_mul_f32 v[138:139], v[214:215], v[134:135] op_sel:[1,0] op_sel_hi:[1,1]
	v_pk_mul_f32 v[140:141], v[214:215], v[154:155] op_sel:[1,0] op_sel_hi:[1,1]
	v_pk_mul_f32 v[142:143], v[214:215], v[156:157] op_sel:[1,0] op_sel_hi:[1,1]
	v_pk_mul_f32 v[190:191], v[46:47], v[136:137]
	v_pk_mul_f32 v[192:193], v[48:49], v[138:139]
	v_pk_mul_f32 v[194:195], v[42:43], v[140:141]
	v_pk_mul_f32 v[196:197], v[44:45], v[142:143]
	v_exp_f32_e32 v190, v190
	v_exp_f32_e32 v191, v191
	v_exp_f32_e32 v192, v192
	v_exp_f32_e32 v193, v193
	v_exp_f32_e32 v194, v194
	v_exp_f32_e32 v195, v195
	v_exp_f32_e32 v196, v196
	v_exp_f32_e32 v197, v197
	v_pk_mul_f32 v[38:39], v[46:47], v[38:39]
	v_pk_mul_f32 v[40:41], v[48:49], v[40:41]
	v_pk_mul_f32 v[34:35], v[42:43], v[34:35]
	v_pk_mul_f32 v[36:37], v[44:45], v[36:37]
	v_pk_mul_f32 v[144:145], v[206:207], v[158:159] op_sel_hi:[0,1]
	v_pk_mul_f32 v[146:147], v[206:207], v[160:161] op_sel_hi:[0,1]
	v_pk_mul_f32 v[148:149], v[206:207], v[186:187] op_sel_hi:[0,1]
	v_pk_mul_f32 v[150:151], v[206:207], v[188:189] op_sel_hi:[0,1]
	v_pk_add_f32 v[190:191], v[190:191], 1.0 op_sel_hi:[1,0]
	v_pk_add_f32 v[192:193], v[192:193], 1.0 op_sel_hi:[1,0]
	v_pk_add_f32 v[194:195], v[194:195], 1.0 op_sel_hi:[1,0]
	v_pk_add_f32 v[196:197], v[196:197], 1.0 op_sel_hi:[1,0]
	v_rcp_f32_e32 v190, v190
	v_rcp_f32_e32 v191, v191
	v_rcp_f32_e32 v192, v192
	v_rcp_f32_e32 v193, v193
	v_rcp_f32_e32 v194, v194
	v_rcp_f32_e32 v195, v195
	v_rcp_f32_e32 v196, v196
	v_rcp_f32_e32 v197, v197
	v_pk_mul_f32 v[38:39], v[38:39], v[144:145]
	v_pk_mul_f32 v[40:41], v[40:41], v[146:147]
	v_pk_mul_f32 v[34:35], v[34:35], v[148:149]
	v_pk_mul_f32 v[36:37], v[36:37], v[150:151]
	s_mov_b32 s100, 0xc6000
	v_pk_mul_f32 v[38:39], v[38:39], v[190:191]
	v_pk_mul_f32 v[40:41], v[40:41], v[192:193]
	v_pk_mul_f32 v[34:35], v[34:35], v[194:195]
	v_pk_mul_f32 v[36:37], v[36:37], v[196:197]
	v_med3_f32 v38, v38, s58, v181
	v_med3_f32 v39, v39, s58, v181
	v_med3_f32 v40, v40, s58, v181
	v_med3_f32 v41, v41, s58, v181
	v_med3_f32 v34, v34, s58, v181
	v_med3_f32 v35, v35, s58, v181
	v_med3_f32 v36, v36, s58, v181
	v_med3_f32 v37, v37, s58, v181
	v_cvt_pk_fp8_f32 v204, v38, v39
	v_cvt_pk_fp8_f32 v205, v34, v35
	v_lshl_add_u64 v[202:203], v[198:199], 0, s[100:101]
	v_cvt_pk_fp8_f32 v204, v40, v41 op_sel:[0,0,1]
	v_cvt_pk_fp8_f32 v205, v36, v37 op_sel:[0,0,1]
	s_nop 0
	global_store_dwordx2 v[202:203], v[204:205], off
	v_cvt_f32_i32_e32 v30, v30
	v_cvt_f32_i32_e32 v31, v31
	v_cvt_f32_i32_e32 v32, v32
	v_cvt_f32_i32_e32 v33, v33
	v_cvt_f32_i32_e32 v26, v26
	v_cvt_f32_i32_e32 v27, v27
	v_cvt_f32_i32_e32 v28, v28
	v_cvt_f32_i32_e32 v29, v29
	v_cvt_f32_i32_e32 v22, v22
	v_cvt_f32_i32_e32 v23, v23
	v_cvt_f32_i32_e32 v24, v24
	v_cvt_f32_i32_e32 v25, v25
	v_cvt_f32_i32_e32 v18, v18
	v_cvt_f32_i32_e32 v19, v19
	v_cvt_f32_i32_e32 v20, v20
	v_cvt_f32_i32_e32 v21, v21
	v_mul_f32_e32 v206, v216, v216
	v_pk_mul_f32 v[136:137], v[216:217], v[132:133] op_sel_hi:[0,1]
	v_pk_mul_f32 v[138:139], v[216:217], v[134:135] op_sel_hi:[0,1]
	v_pk_mul_f32 v[140:141], v[216:217], v[154:155] op_sel_hi:[0,1]
	v_pk_mul_f32 v[142:143], v[216:217], v[156:157] op_sel_hi:[0,1]
	v_pk_mul_f32 v[190:191], v[30:31], v[136:137]
	v_pk_mul_f32 v[192:193], v[32:33], v[138:139]
	v_pk_mul_f32 v[194:195], v[26:27], v[140:141]
	v_pk_mul_f32 v[196:197], v[28:29], v[142:143]
	v_exp_f32_e32 v190, v190
	v_exp_f32_e32 v191, v191
	v_exp_f32_e32 v192, v192
	v_exp_f32_e32 v193, v193
	v_exp_f32_e32 v194, v194
	v_exp_f32_e32 v195, v195
	v_exp_f32_e32 v196, v196
	v_exp_f32_e32 v197, v197
	v_pk_mul_f32 v[22:23], v[30:31], v[22:23]
	v_pk_mul_f32 v[24:25], v[32:33], v[24:25]
	v_pk_mul_f32 v[18:19], v[26:27], v[18:19]
	v_pk_mul_f32 v[20:21], v[28:29], v[20:21]
	v_pk_mul_f32 v[144:145], v[206:207], v[158:159] op_sel_hi:[0,1]
	v_pk_mul_f32 v[146:147], v[206:207], v[160:161] op_sel_hi:[0,1]
; __device__ __forceinline__ unsigned cvt4_fp8(float a, float b, float c, float d) { int w = 0; w = __builtin_amdgcn_cvt_pk_fp8_f32(clamp448(a), clamp448(b), w, false); w = __builtin_amdgcn_cvt_pk_fp8_f32(clamp448(c), clamp448(d), w, true); return (unsigned)w; }
; __device__ __forceinline__ float siluf_(float x) { return x * sigmoidf_(x); }
; __device__ __forceinline__ u32x4 pack8(const f32x4 a, const f32x4 b) { u32x4 w; w.x = cvt_pk_bf16(a[0], a[1]); w.y = cvt_pk_bf16(a[2], a[3]); w.z = cvt_pk_bf16(b[0], b[1]); w.w = cvt_pk_bf16(b[2], b[3]); return w; }
;     __device__ __forceinline__ void operator()(const AccT& acc, const Unit& u, int wr, int wc, int fr, int fq) const {
;     ...
;             for (int m = 0; m < 4; ++m) { const int row = row0 + ai * HALF + m * 16; const float rs = rsc[row]; f32x4 z0, z1;
;                 const i32x4v g0 = __builtin_bit_cast(i32x4v, acc[ai][0][m][0]), g1 = __builtin_bit_cast(i32x4v, acc[ai][0][m][1]), u0 = __builtin_bit_cast(i32x4v, acc[ai][1][m][0]), u1 = __builtin_bit_cast(i32x4v, acc[ai][1][m][1]);
; #pragma unroll
;                 for (int j = 0; j < 4; ++j) { z0[j] = siluf_((float)g0[j] * (rs * cg0[j])) * ((float)u0[j] * (rs * cu0[j])); z1[j] = siluf_((float)g1[j] * (rs * cg1[j])) * ((float)u1[j] * (rs * cu1[j])); }
;                 if (sout8 > 0.f) { u32x2 w; w.x = cvt4_fp8(z0[0] * sout8, z0[1] * sout8, z0[2] * sout8, z0[3] * sout8); w.y = cvt4_fp8(z1[0] * sout8, z1[1] * sout8, z1[2] * sout8, z1[3] * sout8); *(u32x2*)((unsigned char*)O + (size_t)row * ldo + cb) = w; }
;                 else *(u32x4*)(O + (size_t)row * ldo + cb) = pack8(z0, z1);
;                 __builtin_amdgcn_sched_barrier(0); }
	v_pk_mul_f32 v[148:149], v[206:207], v[186:187] op_sel_hi:[0,1]
	v_pk_mul_f32 v[150:151], v[206:207], v[188:189] op_sel_hi:[0,1]
	v_pk_add_f32 v[190:191], v[190:191], 1.0 op_sel_hi:[1,0]
	v_pk_add_f32 v[192:193], v[192:193], 1.0 op_sel_hi:[1,0]
	v_pk_add_f32 v[194:195], v[194:195], 1.0 op_sel_hi:[1,0]
	v_pk_add_f32 v[196:197], v[196:197], 1.0 op_sel_hi:[1,0]
	v_rcp_f32_e32 v190, v190
	v_rcp_f32_e32 v191, v191
	v_rcp_f32_e32 v192, v192
	v_rcp_f32_e32 v193, v193
	v_rcp_f32_e32 v194, v194
	v_rcp_f32_e32 v195, v195
	v_rcp_f32_e32 v196, v196
	v_rcp_f32_e32 v197, v197
	v_pk_mul_f32 v[22:23], v[22:23], v[144:145]
	v_pk_mul_f32 v[24:25], v[24:25], v[146:147]
	v_pk_mul_f32 v[18:19], v[18:19], v[148:149]
	v_pk_mul_f32 v[20:21], v[20:21], v[150:151]
	s_mov_b32 s100, 0xdc000
	v_pk_mul_f32 v[22:23], v[22:23], v[190:191]
	v_pk_mul_f32 v[24:25], v[24:25], v[192:193]
	v_pk_mul_f32 v[18:19], v[18:19], v[194:195]
	v_pk_mul_f32 v[20:21], v[20:21], v[196:197]
	v_med3_f32 v22, v22, s58, v181
	v_med3_f32 v23, v23, s58, v181
	v_med3_f32 v24, v24, s58, v181
	v_med3_f32 v25, v25, s58, v181
	v_med3_f32 v18, v18, s58, v181
	v_med3_f32 v19, v19, s58, v181
	v_med3_f32 v20, v20, s58, v181
	v_med3_f32 v21, v21, s58, v181
	v_cvt_pk_fp8_f32 v204, v22, v23
	v_cvt_pk_fp8_f32 v205, v18, v19
	v_lshl_add_u64 v[202:203], v[198:199], 0, s[100:101]
	v_cvt_pk_fp8_f32 v204, v24, v25 op_sel:[0,0,1]
	v_cvt_pk_fp8_f32 v205, v20, v21 op_sel:[0,0,1]
	s_nop 0
	global_store_dwordx2 v[202:203], v[204:205], off
	v_cvt_f32_i32_e32 v14, v14
	v_cvt_f32_i32_e32 v15, v15
	v_cvt_f32_i32_e32 v16, v16
	v_cvt_f32_i32_e32 v17, v17
	v_cvt_f32_i32_e32 v10, v10
	v_cvt_f32_i32_e32 v11, v11
	v_cvt_f32_i32_e32 v12, v12
	v_cvt_f32_i32_e32 v13, v13
	v_cvt_f32_i32_e32 v6, v6
	v_cvt_f32_i32_e32 v7, v7
	v_cvt_f32_i32_e32 v8, v8
	v_cvt_f32_i32_e32 v9, v9
	v_cvt_f32_i32_e32 v2, v2
	v_cvt_f32_i32_e32 v3, v3
	v_cvt_f32_i32_e32 v4, v4
	v_cvt_f32_i32_e32 v5, v5
	v_mul_f32_e32 v206, v217, v217
	v_pk_mul_f32 v[136:137], v[216:217], v[132:133] op_sel:[1,0] op_sel_hi:[1,1]
	v_pk_mul_f32 v[138:139], v[216:217], v[134:135] op_sel:[1,0] op_sel_hi:[1,1]
	v_pk_mul_f32 v[140:141], v[216:217], v[154:155] op_sel:[1,0] op_sel_hi:[1,1]
	v_pk_mul_f32 v[142:143], v[216:217], v[156:157] op_sel:[1,0] op_sel_hi:[1,1]
	v_pk_mul_f32 v[190:191], v[14:15], v[136:137]
	v_pk_mul_f32 v[192:193], v[16:17], v[138:139]
	v_pk_mul_f32 v[194:195], v[10:11], v[140:141]
	v_pk_mul_f32 v[196:197], v[12:13], v[142:143]
	v_exp_f32_e32 v190, v190
	v_exp_f32_e32 v191, v191
	v_exp_f32_e32 v192, v192
	v_exp_f32_e32 v193, v193
	v_exp_f32_e32 v194, v194
	v_exp_f32_e32 v195, v195
	v_exp_f32_e32 v196, v196
	v_exp_f32_e32 v197, v197
	v_pk_mul_f32 v[6:7], v[14:15], v[6:7]
	v_pk_mul_f32 v[8:9], v[16:17], v[8:9]
	v_pk_mul_f32 v[2:3], v[10:11], v[2:3]
	v_pk_mul_f32 v[4:5], v[12:13], v[4:5]
	v_pk_mul_f32 v[144:145], v[206:207], v[158:159] op_sel_hi:[0,1]
	v_pk_mul_f32 v[146:147], v[206:207], v[160:161] op_sel_hi:[0,1]
	v_pk_mul_f32 v[148:149], v[206:207], v[186:187] op_sel_hi:[0,1]
	v_pk_mul_f32 v[150:151], v[206:207], v[188:189] op_sel_hi:[0,1]
	v_pk_add_f32 v[190:191], v[190:191], 1.0 op_sel_hi:[1,0]
	v_pk_add_f32 v[192:193], v[192:193], 1.0 op_sel_hi:[1,0]
	v_pk_add_f32 v[194:195], v[194:195], 1.0 op_sel_hi:[1,0]
	v_pk_add_f32 v[196:197], v[196:197], 1.0 op_sel_hi:[1,0]
	v_rcp_f32_e32 v190, v190
	v_rcp_f32_e32 v191, v191
	v_rcp_f32_e32 v192, v192
	v_rcp_f32_e32 v193, v193
	v_rcp_f32_e32 v194, v194
	v_rcp_f32_e32 v195, v195
	v_rcp_f32_e32 v196, v196
	v_rcp_f32_e32 v197, v197
	v_pk_mul_f32 v[6:7], v[6:7], v[144:145]
	v_pk_mul_f32 v[8:9], v[8:9], v[146:147]
	v_pk_mul_f32 v[2:3], v[2:3], v[148:149]
	v_pk_mul_f32 v[4:5], v[4:5], v[150:151]
	s_mov_b32 s100, 0xf2000
	v_pk_mul_f32 v[6:7], v[6:7], v[190:191]
	v_pk_mul_f32 v[8:9], v[8:9], v[192:193]
	v_pk_mul_f32 v[2:3], v[2:3], v[194:195]
	v_pk_mul_f32 v[4:5], v[4:5], v[196:197]
	v_med3_f32 v6, v6, s58, v181
	v_med3_f32 v7, v7, s58, v181
	v_med3_f32 v8, v8, s58, v181
	v_med3_f32 v9, v9, s58, v181
	v_med3_f32 v2, v2, s58, v181
	v_med3_f32 v3, v3, s58, v181
	v_med3_f32 v4, v4, s58, v181
	v_med3_f32 v5, v5, s58, v181
	v_cvt_pk_fp8_f32 v204, v6, v7
	v_cvt_pk_fp8_f32 v205, v2, v3
	v_lshl_add_u64 v[202:203], v[198:199], 0, s[100:101]
	v_cvt_pk_fp8_f32 v204, v8, v9 op_sel:[0,0,1]
	v_cvt_pk_fp8_f32 v205, v4, v5 op_sel:[0,0,1]
	s_nop 0
	global_store_dwordx2 v[202:203], v[204:205], off
	s_andn2_b64 vcc, exec, s[28:29]
	s_mov_b64 s[28:29], -1
	s_cbranch_vccnz .LBB0_1408
	s_andn2_b64 vcc, exec, s[4:5]
	s_cbranch_vccnz .LBB0_1407
	s_barrier
	s_branch .LBB0_1407

; __device__ __forceinline__ unsigned cvt4_fp8(float a, float b, float c, float d) { int w = 0; w = __builtin_amdgcn_cvt_pk_fp8_f32(clamp448(a), clamp448(b), w, false); w = __builtin_amdgcn_cvt_pk_fp8_f32(clamp448(c), clamp448(d), w, true); return (unsigned)w; }
; __device__ __forceinline__ float sigmoidf_(float x) { return __builtin_amdgcn_rcpf(1.0f + __expf(-x)); }
; __device__ __forceinline__ float siluf_(float x) { return x * sigmoidf_(x); }
;     __device__ __forceinline__ void operator()(const AccT& acc, const Unit& u, int wr, int wc, int fr, int fq) const {
;         const int rl0 = wr * 64 + fr, cb = u.pn * 128 + wc * 32 + 8 * fq, nb = u.g * 14336 + u.pn * 256 + wc * 32 + 8 * fq;
;         const float* rs_p = rsc + (size_t)u.g * ML + u.pm * BM;
;         f32x4 cg0 = *(const f32x4*)(cmax + nb) * (1.0f / 127.0f), cg1 = *(const f32x4*)(cmax + nb + 4) * (1.0f / 127.0f), cu0 = *(const f32x4*)(cmax + nb + 128) * (1.0f / 127.0f), cu1 = *(const f32x4*)(cmax + nb + 132) * (1.0f / 127.0f);
; #pragma unroll
;         for (int ai = 0; ai < 2; ++ai)
; #pragma unroll
;             for (int m = 0; m < 4; ++m) { const int rl = rl0 + ai * HALF + m * 16; const float rs = rs_p[rl]; f32x4 z0, z1;
;                 const i32x4v g0 = __builtin_bit_cast(i32x4v, acc[ai][0][m][0]), g1 = __builtin_bit_cast(i32x4v, acc[ai][0][m][1]), u0 = __builtin_bit_cast(i32x4v, acc[ai][1][m][0]), u1 = __builtin_bit_cast(i32x4v, acc[ai][1][m][1]);
; #pragma unroll
;                 for (int j = 0; j < 4; ++j) { z0[j] = siluf_((float)g0[j] * (rs * cg0[j])) * ((float)u0[j] * (rs * cu0[j])); z1[j] = siluf_((float)g1[j] * (rs * cg1[j])) * ((float)u1[j] * (rs * cu1[j])); }
;                 u32x2 w; w.x = cvt4_fp8(z0[0] * sout8, z0[1] * sout8, z0[2] * sout8, z0[3] * sout8); w.y = cvt4_fp8(z1[0] * sout8, z1[1] * sout8, z1[2] * sout8, z1[3] * sout8);
;                 *(u32x2*)(O + (size_t)(u.orow0 + rl) * ldo + cb) = w;
;                 __builtin_amdgcn_sched_barrier(0); }
.LBB0_2553:
	v_mul_lo_u32 v130, v168, s70
	s_lshl_b32 s4, s44, 8
	v_add_u32_e32 v130, s4, v130
	v_or_b32_e32 v130, v130, v183
	v_ashrrev_i32_e32 v131, 31, v130
	v_lshl_add_u64 v[130:131], v[130:131], 2, s[24:25]
	v_ashrrev_i32_e32 v169, 31, v168
	s_lshl_b32 s4, s74, 8
	global_load_dwordx4 v[134:137], v[130:131], off offset:512
	global_load_dwordx4 v[138:141], v[130:131], off
	global_load_dwordx4 v[142:145], v[130:131], off offset:528
	global_load_dwordx4 v[146:149], v[130:131], off offset:16
	v_lshlrev_b64 v[130:131], 16, v[168:169]
	s_ashr_i32 s5, s4, 31
	v_lshl_add_u64 v[130:131], s[22:23], 0, v[130:131]
	s_lshl_b64 s[4:5], s[4:5], 2
	v_lshl_add_u64 v[132:133], v[130:131], 0, s[4:5]
	s_nop 0
	v_readfirstlane_b32 s4, v132
	v_readfirstlane_b32 s5, v133
	s_nop 0
	s_nop 0
	s_nop 0
	s_nop 0
	s_nop 0
	global_load_dword v150, v185, s[4:5]
	global_load_dword v219, v185, s[4:5] offset:64
	global_load_dword v220, v185, s[4:5] offset:128
	global_load_dword v221, v185, s[4:5] offset:192
	global_load_dword v222, v185, s[4:5] offset:512
	global_load_dword v223, v185, s[4:5] offset:576
	global_load_dword v224, v185, s[4:5] offset:640
	global_load_dword v225, v185, s[4:5] offset:704
	s_nop 0
	s_nop 0
	s_nop 0
	s_nop 0
	s_nop 0
	s_nop 0
	s_nop 0
	s_nop 0
	v_lshl_or_b32 v130, s44, 7, v183
	v_ashrrev_i32_e32 v131, 31, v130
	s_waitcnt vmcnt(0)
	s_mov_b32 s98, 0xbc3a1e78
	s_mov_b32 s100, 0x39820610
	v_pk_mul_f32 v[132:133], v[138:139], s[98:99] op_sel_hi:[1,0]
	v_pk_mul_f32 v[152:153], v[140:141], s[98:99] op_sel_hi:[1,0]
	v_pk_mul_f32 v[154:155], v[146:147], s[98:99] op_sel_hi:[1,0]
	v_pk_mul_f32 v[156:157], v[148:149], s[98:99] op_sel_hi:[1,0]
	v_pk_mul_f32 v[158:159], v[138:139], v[134:135]
	v_pk_mul_f32 v[160:161], v[140:141], v[136:137]
	v_pk_mul_f32 v[194:195], v[146:147], v[142:143]
	v_pk_mul_f32 v[196:197], v[148:149], v[144:145]
	v_add_u32_e32 v215, v190, v164
	v_mov_b64_e32 v[208:209], s[20:21]
	v_pk_mul_f32 v[158:159], v[158:159], s[100:101] op_sel_hi:[1,0]
	v_pk_mul_f32 v[160:161], v[160:161], s[100:101] op_sel_hi:[1,0]
	v_pk_mul_f32 v[194:195], v[194:195], s[100:101] op_sel_hi:[1,0]
	v_pk_mul_f32 v[196:197], v[196:197], s[100:101] op_sel_hi:[1,0]
	v_mad_i64_i32 v[206:207], s[6:7], v215, s72, v[208:209]
	v_lshl_add_u64 v[206:207], v[206:207], 0, v[130:131]
	s_mov_b32 s5, 0
	v_cvt_f32_i32_e32 v126, v126
	v_cvt_f32_i32_e32 v127, v127
	v_cvt_f32_i32_e32 v128, v128
	v_cvt_f32_i32_e32 v129, v129
	v_cvt_f32_i32_e32 v118, v118
	v_cvt_f32_i32_e32 v119, v119
	v_cvt_f32_i32_e32 v120, v120
	v_cvt_f32_i32_e32 v121, v121
	v_cvt_f32_i32_e32 v122, v122
	v_cvt_f32_i32_e32 v123, v123
	v_cvt_f32_i32_e32 v124, v124
	v_cvt_f32_i32_e32 v125, v125
	v_cvt_f32_i32_e32 v114, v114
	v_cvt_f32_i32_e32 v115, v115
	v_cvt_f32_i32_e32 v116, v116
	v_cvt_f32_i32_e32 v117, v117
	v_mul_f32_e32 v214, v150, v150
	v_pk_mul_f32 v[134:135], v[150:151], v[132:133] op_sel_hi:[0,1]
	v_pk_mul_f32 v[136:137], v[150:151], v[152:153] op_sel_hi:[0,1]
	v_pk_mul_f32 v[138:139], v[150:151], v[154:155] op_sel_hi:[0,1]
	v_pk_mul_f32 v[140:141], v[150:151], v[156:157] op_sel_hi:[0,1]
	v_pk_mul_f32 v[198:199], v[126:127], v[134:135]
	v_pk_mul_f32 v[200:201], v[128:129], v[136:137]
	v_pk_mul_f32 v[202:203], v[118:119], v[138:139]
	v_pk_mul_f32 v[204:205], v[120:121], v[140:141]
	v_exp_f32_e32 v198, v198
	v_exp_f32_e32 v199, v199
	v_exp_f32_e32 v200, v200
	v_exp_f32_e32 v201, v201
	v_exp_f32_e32 v202, v202
	v_exp_f32_e32 v203, v203
	v_exp_f32_e32 v204, v204
	v_exp_f32_e32 v205, v205
	v_pk_mul_f32 v[122:123], v[126:127], v[122:123]
	v_pk_mul_f32 v[124:125], v[128:129], v[124:125]
	v_pk_mul_f32 v[114:115], v[118:119], v[114:115]
	v_pk_mul_f32 v[116:117], v[120:121], v[116:117]
	v_pk_mul_f32 v[142:143], v[214:215], v[158:159] op_sel_hi:[0,1]
	v_pk_mul_f32 v[144:145], v[214:215], v[160:161] op_sel_hi:[0,1]
	v_pk_mul_f32 v[146:147], v[214:215], v[194:195] op_sel_hi:[0,1]
	v_pk_mul_f32 v[148:149], v[214:215], v[196:197] op_sel_hi:[0,1]
	v_pk_add_f32 v[198:199], v[198:199], 1.0 op_sel_hi:[1,0]
	v_pk_add_f32 v[200:201], v[200:201], 1.0 op_sel_hi:[1,0]
	v_pk_add_f32 v[202:203], v[202:203], 1.0 op_sel_hi:[1,0]
	v_pk_add_f32 v[204:205], v[204:205], 1.0 op_sel_hi:[1,0]
	v_rcp_f32_e32 v198, v198
	v_rcp_f32_e32 v199, v199
	v_rcp_f32_e32 v200, v200
	v_rcp_f32_e32 v201, v201
	v_rcp_f32_e32 v202, v202
	v_rcp_f32_e32 v203, v203
	v_rcp_f32_e32 v204, v204
	v_rcp_f32_e32 v205, v205
	v_pk_mul_f32 v[122:123], v[122:123], v[142:143]
	v_pk_mul_f32 v[124:125], v[124:125], v[144:145]
	v_pk_mul_f32 v[114:115], v[114:115], v[146:147]
	v_pk_mul_f32 v[116:117], v[116:117], v[148:149]
	s_mov_b32 s4, 0x0
	v_pk_mul_f32 v[122:123], v[122:123], v[198:199]
	v_pk_mul_f32 v[124:125], v[124:125], v[200:201]
	v_pk_mul_f32 v[114:115], v[114:115], v[202:203]
	v_pk_mul_f32 v[116:117], v[116:117], v[204:205]
	v_med3_f32 v122, v122, s71, v187
	v_med3_f32 v123, v123, s71, v187
	v_med3_f32 v124, v124, s71, v187
	v_med3_f32 v125, v125, s71, v187
	v_med3_f32 v114, v114, s71, v187
	v_med3_f32 v115, v115, s71, v187
	v_med3_f32 v116, v116, s71, v187
	v_med3_f32 v117, v117, s71, v187
	v_cvt_pk_fp8_f32 v212, v122, v123
	v_cvt_pk_fp8_f32 v213, v114, v115
	v_lshl_add_u64 v[210:211], v[206:207], 0, s[4:5]
	v_cvt_pk_fp8_f32 v212, v124, v125 op_sel:[0,0,1]
	v_cvt_pk_fp8_f32 v213, v116, v117 op_sel:[0,0,1]
	s_nop 0
	global_store_dwordx2 v[210:211], v[212:213], off
	v_cvt_f32_i32_e32 v110, v110
	v_cvt_f32_i32_e32 v111, v111
	v_cvt_f32_i32_e32 v112, v112
	v_cvt_f32_i32_e32 v113, v113
	v_cvt_f32_i32_e32 v106, v106
	v_cvt_f32_i32_e32 v107, v107
	v_cvt_f32_i32_e32 v108, v108
	v_cvt_f32_i32_e32 v109, v109
	v_cvt_f32_i32_e32 v102, v102
	v_cvt_f32_i32_e32 v103, v103
; __device__ __forceinline__ unsigned cvt4_fp8(float a, float b, float c, float d) { int w = 0; w = __builtin_amdgcn_cvt_pk_fp8_f32(clamp448(a), clamp448(b), w, false); w = __builtin_amdgcn_cvt_pk_fp8_f32(clamp448(c), clamp448(d), w, true); return (unsigned)w; }
; __device__ __forceinline__ float sigmoidf_(float x) { return __builtin_amdgcn_rcpf(1.0f + __expf(-x)); }
; __device__ __forceinline__ float siluf_(float x) { return x * sigmoidf_(x); }
;     __device__ __forceinline__ void operator()(const AccT& acc, const Unit& u, int wr, int wc, int fr, int fq) const {
;     ...
;             for (int m = 0; m < 4; ++m) { const int rl = rl0 + ai * HALF + m * 16; const float rs = rs_p[rl]; f32x4 z0, z1;
;                 const i32x4v g0 = __builtin_bit_cast(i32x4v, acc[ai][0][m][0]), g1 = __builtin_bit_cast(i32x4v, acc[ai][0][m][1]), u0 = __builtin_bit_cast(i32x4v, acc[ai][1][m][0]), u1 = __builtin_bit_cast(i32x4v, acc[ai][1][m][1]);
; #pragma unroll
;                 for (int j = 0; j < 4; ++j) { z0[j] = siluf_((float)g0[j] * (rs * cg0[j])) * ((float)u0[j] * (rs * cu0[j])); z1[j] = siluf_((float)g1[j] * (rs * cg1[j])) * ((float)u1[j] * (rs * cu1[j])); }
;                 u32x2 w; w.x = cvt4_fp8(z0[0] * sout8, z0[1] * sout8, z0[2] * sout8, z0[3] * sout8); w.y = cvt4_fp8(z1[0] * sout8, z1[1] * sout8, z1[2] * sout8, z1[3] * sout8);
;                 *(u32x2*)(O + (size_t)(u.orow0 + rl) * ldo + cb) = w;
;                 __builtin_amdgcn_sched_barrier(0); }
	v_cvt_f32_i32_e32 v104, v104
	v_cvt_f32_i32_e32 v105, v105
	v_cvt_f32_i32_e32 v98, v98
	v_cvt_f32_i32_e32 v99, v99
	v_cvt_f32_i32_e32 v100, v100
	v_cvt_f32_i32_e32 v101, v101
	v_mul_f32_e32 v214, v219, v219
	v_pk_mul_f32 v[134:135], v[218:219], v[132:133] op_sel:[1,0] op_sel_hi:[1,1]
	v_pk_mul_f32 v[136:137], v[218:219], v[152:153] op_sel:[1,0] op_sel_hi:[1,1]
	v_pk_mul_f32 v[138:139], v[218:219], v[154:155] op_sel:[1,0] op_sel_hi:[1,1]
	v_pk_mul_f32 v[140:141], v[218:219], v[156:157] op_sel:[1,0] op_sel_hi:[1,1]
	v_pk_mul_f32 v[198:199], v[110:111], v[134:135]
	v_pk_mul_f32 v[200:201], v[112:113], v[136:137]
	v_pk_mul_f32 v[202:203], v[106:107], v[138:139]
	v_pk_mul_f32 v[204:205], v[108:109], v[140:141]
	v_exp_f32_e32 v198, v198
	v_exp_f32_e32 v199, v199
	v_exp_f32_e32 v200, v200
	v_exp_f32_e32 v201, v201
	v_exp_f32_e32 v202, v202
	v_exp_f32_e32 v203, v203
	v_exp_f32_e32 v204, v204
	v_exp_f32_e32 v205, v205
	v_pk_mul_f32 v[102:103], v[110:111], v[102:103]
	v_pk_mul_f32 v[104:105], v[112:113], v[104:105]
	v_pk_mul_f32 v[98:99], v[106:107], v[98:99]
	v_pk_mul_f32 v[100:101], v[108:109], v[100:101]
	v_pk_mul_f32 v[142:143], v[214:215], v[158:159] op_sel_hi:[0,1]
	v_pk_mul_f32 v[144:145], v[214:215], v[160:161] op_sel_hi:[0,1]
	v_pk_mul_f32 v[146:147], v[214:215], v[194:195] op_sel_hi:[0,1]
	v_pk_mul_f32 v[148:149], v[214:215], v[196:197] op_sel_hi:[0,1]
	v_pk_add_f32 v[198:199], v[198:199], 1.0 op_sel_hi:[1,0]
	v_pk_add_f32 v[200:201], v[200:201], 1.0 op_sel_hi:[1,0]
	v_pk_add_f32 v[202:203], v[202:203], 1.0 op_sel_hi:[1,0]
	v_pk_add_f32 v[204:205], v[204:205], 1.0 op_sel_hi:[1,0]
	v_rcp_f32_e32 v198, v198
	v_rcp_f32_e32 v199, v199
	v_rcp_f32_e32 v200, v200
	v_rcp_f32_e32 v201, v201
	v_rcp_f32_e32 v202, v202
	v_rcp_f32_e32 v203, v203
	v_rcp_f32_e32 v204, v204
	v_rcp_f32_e32 v205, v205
	v_pk_mul_f32 v[102:103], v[102:103], v[142:143]
	v_pk_mul_f32 v[104:105], v[104:105], v[144:145]
	v_pk_mul_f32 v[98:99], v[98:99], v[146:147]
	v_pk_mul_f32 v[100:101], v[100:101], v[148:149]
	s_mov_b32 s4, 0x1c000
	v_pk_mul_f32 v[102:103], v[102:103], v[198:199]
	v_pk_mul_f32 v[104:105], v[104:105], v[200:201]
	v_pk_mul_f32 v[98:99], v[98:99], v[202:203]
	v_pk_mul_f32 v[100:101], v[100:101], v[204:205]
	v_med3_f32 v102, v102, s71, v187
	v_med3_f32 v103, v103, s71, v187
	v_med3_f32 v104, v104, s71, v187
	v_med3_f32 v105, v105, s71, v187
	v_med3_f32 v98, v98, s71, v187
	v_med3_f32 v99, v99, s71, v187
	v_med3_f32 v100, v100, s71, v187
	v_med3_f32 v101, v101, s71, v187
	v_cvt_pk_fp8_f32 v212, v102, v103
	v_cvt_pk_fp8_f32 v213, v98, v99
	v_lshl_add_u64 v[210:211], v[206:207], 0, s[4:5]
	v_cvt_pk_fp8_f32 v212, v104, v105 op_sel:[0,0,1]
	v_cvt_pk_fp8_f32 v213, v100, v101 op_sel:[0,0,1]
	s_nop 0
	global_store_dwordx2 v[210:211], v[212:213], off
	v_cvt_f32_i32_e32 v94, v94
	v_cvt_f32_i32_e32 v95, v95
	v_cvt_f32_i32_e32 v96, v96
	v_cvt_f32_i32_e32 v97, v97
	v_cvt_f32_i32_e32 v90, v90
	v_cvt_f32_i32_e32 v91, v91
	v_cvt_f32_i32_e32 v92, v92
	v_cvt_f32_i32_e32 v93, v93
	v_cvt_f32_i32_e32 v86, v86
	v_cvt_f32_i32_e32 v87, v87
	v_cvt_f32_i32_e32 v88, v88
	v_cvt_f32_i32_e32 v89, v89
	v_cvt_f32_i32_e32 v82, v82
	v_cvt_f32_i32_e32 v83, v83
	v_cvt_f32_i32_e32 v84, v84
	v_cvt_f32_i32_e32 v85, v85
	v_mul_f32_e32 v214, v220, v220
	v_pk_mul_f32 v[134:135], v[220:221], v[132:133] op_sel_hi:[0,1]
	v_pk_mul_f32 v[136:137], v[220:221], v[152:153] op_sel_hi:[0,1]
	v_pk_mul_f32 v[138:139], v[220:221], v[154:155] op_sel_hi:[0,1]
	v_pk_mul_f32 v[140:141], v[220:221], v[156:157] op_sel_hi:[0,1]
	v_pk_mul_f32 v[198:199], v[94:95], v[134:135]
	v_pk_mul_f32 v[200:201], v[96:97], v[136:137]
	v_pk_mul_f32 v[202:203], v[90:91], v[138:139]
	v_pk_mul_f32 v[204:205], v[92:93], v[140:141]
	v_exp_f32_e32 v198, v198
	v_exp_f32_e32 v199, v199
	v_exp_f32_e32 v200, v200
	v_exp_f32_e32 v201, v201
	v_exp_f32_e32 v202, v202
	v_exp_f32_e32 v203, v203
	v_exp_f32_e32 v204, v204
	v_exp_f32_e32 v205, v205
	v_pk_mul_f32 v[86:87], v[94:95], v[86:87]
	v_pk_mul_f32 v[88:89], v[96:97], v[88:89]
	v_pk_mul_f32 v[82:83], v[90:91], v[82:83]
	v_pk_mul_f32 v[84:85], v[92:93], v[84:85]
	v_pk_mul_f32 v[142:143], v[214:215], v[158:159] op_sel_hi:[0,1]
	v_pk_mul_f32 v[144:145], v[214:215], v[160:161] op_sel_hi:[0,1]
	v_pk_mul_f32 v[146:147], v[214:215], v[194:195] op_sel_hi:[0,1]
	v_pk_mul_f32 v[148:149], v[214:215], v[196:197] op_sel_hi:[0,1]
	v_pk_add_f32 v[198:199], v[198:199], 1.0 op_sel_hi:[1,0]
	v_pk_add_f32 v[200:201], v[200:201], 1.0 op_sel_hi:[1,0]
	v_pk_add_f32 v[202:203], v[202:203], 1.0 op_sel_hi:[1,0]
	v_pk_add_f32 v[204:205], v[204:205], 1.0 op_sel_hi:[1,0]
	v_rcp_f32_e32 v198, v198
	v_rcp_f32_e32 v199, v199
	v_rcp_f32_e32 v200, v200
	v_rcp_f32_e32 v201, v201
	v_rcp_f32_e32 v202, v202
	v_rcp_f32_e32 v203, v203
	v_rcp_f32_e32 v204, v204
	v_rcp_f32_e32 v205, v205
	v_pk_mul_f32 v[86:87], v[86:87], v[142:143]
	v_pk_mul_f32 v[88:89], v[88:89], v[144:145]
	v_pk_mul_f32 v[82:83], v[82:83], v[146:147]
	v_pk_mul_f32 v[84:85], v[84:85], v[148:149]
	s_mov_b32 s4, 0x38000
	v_pk_mul_f32 v[86:87], v[86:87], v[198:199]
	v_pk_mul_f32 v[88:89], v[88:89], v[200:201]
	v_pk_mul_f32 v[82:83], v[82:83], v[202:203]
	v_pk_mul_f32 v[84:85], v[84:85], v[204:205]
	v_med3_f32 v86, v86, s71, v187
	v_med3_f32 v87, v87, s71, v187
	v_med3_f32 v88, v88, s71, v187
	v_med3_f32 v89, v89, s71, v187
	v_med3_f32 v82, v82, s71, v187
	v_med3_f32 v83, v83, s71, v187
	v_med3_f32 v84, v84, s71, v187
	v_med3_f32 v85, v85, s71, v187
	v_cvt_pk_fp8_f32 v212, v86, v87
	v_cvt_pk_fp8_f32 v213, v82, v83
	v_lshl_add_u64 v[210:211], v[206:207], 0, s[4:5]
	v_cvt_pk_fp8_f32 v212, v88, v89 op_sel:[0,0,1]
	v_cvt_pk_fp8_f32 v213, v84, v85 op_sel:[0,0,1]
	s_nop 0
; __device__ __forceinline__ unsigned cvt4_fp8(float a, float b, float c, float d) { int w = 0; w = __builtin_amdgcn_cvt_pk_fp8_f32(clamp448(a), clamp448(b), w, false); w = __builtin_amdgcn_cvt_pk_fp8_f32(clamp448(c), clamp448(d), w, true); return (unsigned)w; }
; __device__ __forceinline__ float siluf_(float x) { return x * sigmoidf_(x); }
;     __device__ __forceinline__ void operator()(const AccT& acc, const Unit& u, int wr, int wc, int fr, int fq) const {
;     ...
;             for (int m = 0; m < 4; ++m) { const int rl = rl0 + ai * HALF + m * 16; const float rs = rs_p[rl]; f32x4 z0, z1;
;                 const i32x4v g0 = __builtin_bit_cast(i32x4v, acc[ai][0][m][0]), g1 = __builtin_bit_cast(i32x4v, acc[ai][0][m][1]), u0 = __builtin_bit_cast(i32x4v, acc[ai][1][m][0]), u1 = __builtin_bit_cast(i32x4v, acc[ai][1][m][1]);
; #pragma unroll
;                 for (int j = 0; j < 4; ++j) { z0[j] = siluf_((float)g0[j] * (rs * cg0[j])) * ((float)u0[j] * (rs * cu0[j])); z1[j] = siluf_((float)g1[j] * (rs * cg1[j])) * ((float)u1[j] * (rs * cu1[j])); }
;                 u32x2 w; w.x = cvt4_fp8(z0[0] * sout8, z0[1] * sout8, z0[2] * sout8, z0[3] * sout8); w.y = cvt4_fp8(z1[0] * sout8, z1[1] * sout8, z1[2] * sout8, z1[3] * sout8);
;                 *(u32x2*)(O + (size_t)(u.orow0 + rl) * ldo + cb) = w;
;                 __builtin_amdgcn_sched_barrier(0); }
	global_store_dwordx2 v[210:211], v[212:213], off
	v_cvt_f32_i32_e32 v78, v78
	v_cvt_f32_i32_e32 v79, v79
	v_cvt_f32_i32_e32 v80, v80
	v_cvt_f32_i32_e32 v81, v81
	v_cvt_f32_i32_e32 v74, v74
	v_cvt_f32_i32_e32 v75, v75
	v_cvt_f32_i32_e32 v76, v76
	v_cvt_f32_i32_e32 v77, v77
	v_cvt_f32_i32_e32 v70, v70
	v_cvt_f32_i32_e32 v71, v71
	v_cvt_f32_i32_e32 v72, v72
	v_cvt_f32_i32_e32 v73, v73
	v_cvt_f32_i32_e32 v66, v66
	v_cvt_f32_i32_e32 v67, v67
	v_cvt_f32_i32_e32 v68, v68
	v_cvt_f32_i32_e32 v69, v69
	v_mul_f32_e32 v214, v221, v221
	v_pk_mul_f32 v[134:135], v[220:221], v[132:133] op_sel:[1,0] op_sel_hi:[1,1]
	v_pk_mul_f32 v[136:137], v[220:221], v[152:153] op_sel:[1,0] op_sel_hi:[1,1]
	v_pk_mul_f32 v[138:139], v[220:221], v[154:155] op_sel:[1,0] op_sel_hi:[1,1]
	v_pk_mul_f32 v[140:141], v[220:221], v[156:157] op_sel:[1,0] op_sel_hi:[1,1]
	v_pk_mul_f32 v[198:199], v[78:79], v[134:135]
	v_pk_mul_f32 v[200:201], v[80:81], v[136:137]
	v_pk_mul_f32 v[202:203], v[74:75], v[138:139]
	v_pk_mul_f32 v[204:205], v[76:77], v[140:141]
	v_exp_f32_e32 v198, v198
	v_exp_f32_e32 v199, v199
	v_exp_f32_e32 v200, v200
	v_exp_f32_e32 v201, v201
	v_exp_f32_e32 v202, v202
	v_exp_f32_e32 v203, v203
	v_exp_f32_e32 v204, v204
	v_exp_f32_e32 v205, v205
	v_pk_mul_f32 v[70:71], v[78:79], v[70:71]
	v_pk_mul_f32 v[72:73], v[80:81], v[72:73]
	v_pk_mul_f32 v[66:67], v[74:75], v[66:67]
	v_pk_mul_f32 v[68:69], v[76:77], v[68:69]
	v_pk_mul_f32 v[142:143], v[214:215], v[158:159] op_sel_hi:[0,1]
	v_pk_mul_f32 v[144:145], v[214:215], v[160:161] op_sel_hi:[0,1]
	v_pk_mul_f32 v[146:147], v[214:215], v[194:195] op_sel_hi:[0,1]
	v_pk_mul_f32 v[148:149], v[214:215], v[196:197] op_sel_hi:[0,1]
	v_pk_add_f32 v[198:199], v[198:199], 1.0 op_sel_hi:[1,0]
	v_pk_add_f32 v[200:201], v[200:201], 1.0 op_sel_hi:[1,0]
	v_pk_add_f32 v[202:203], v[202:203], 1.0 op_sel_hi:[1,0]
	v_pk_add_f32 v[204:205], v[204:205], 1.0 op_sel_hi:[1,0]
	v_rcp_f32_e32 v198, v198
	v_rcp_f32_e32 v199, v199
	v_rcp_f32_e32 v200, v200
	v_rcp_f32_e32 v201, v201
	v_rcp_f32_e32 v202, v202
	v_rcp_f32_e32 v203, v203
	v_rcp_f32_e32 v204, v204
	v_rcp_f32_e32 v205, v205
	v_pk_mul_f32 v[70:71], v[70:71], v[142:143]
	v_pk_mul_f32 v[72:73], v[72:73], v[144:145]
	v_pk_mul_f32 v[66:67], v[66:67], v[146:147]
	v_pk_mul_f32 v[68:69], v[68:69], v[148:149]
	s_mov_b32 s4, 0x54000
	v_pk_mul_f32 v[70:71], v[70:71], v[198:199]
	v_pk_mul_f32 v[72:73], v[72:73], v[200:201]
	v_pk_mul_f32 v[66:67], v[66:67], v[202:203]
	v_pk_mul_f32 v[68:69], v[68:69], v[204:205]
	v_med3_f32 v70, v70, s71, v187
	v_med3_f32 v71, v71, s71, v187
	v_med3_f32 v72, v72, s71, v187
	v_med3_f32 v73, v73, s71, v187
	v_med3_f32 v66, v66, s71, v187
	v_med3_f32 v67, v67, s71, v187
	v_med3_f32 v68, v68, s71, v187
	v_med3_f32 v69, v69, s71, v187
	v_cvt_pk_fp8_f32 v212, v70, v71
	v_cvt_pk_fp8_f32 v213, v66, v67
	v_lshl_add_u64 v[210:211], v[206:207], 0, s[4:5]
	v_cvt_pk_fp8_f32 v212, v72, v73 op_sel:[0,0,1]
	v_cvt_pk_fp8_f32 v213, v68, v69 op_sel:[0,0,1]
	s_nop 0
	global_store_dwordx2 v[210:211], v[212:213], off
	v_cvt_f32_i32_e32 v62, v62
	v_cvt_f32_i32_e32 v63, v63
	v_cvt_f32_i32_e32 v64, v64
	v_cvt_f32_i32_e32 v65, v65
	v_cvt_f32_i32_e32 v58, v58
	v_cvt_f32_i32_e32 v59, v59
	v_cvt_f32_i32_e32 v60, v60
	v_cvt_f32_i32_e32 v61, v61
	v_cvt_f32_i32_e32 v54, v54
	v_cvt_f32_i32_e32 v55, v55
	v_cvt_f32_i32_e32 v56, v56
	v_cvt_f32_i32_e32 v57, v57
	v_cvt_f32_i32_e32 v50, v50
	v_cvt_f32_i32_e32 v51, v51
	v_cvt_f32_i32_e32 v52, v52
	v_cvt_f32_i32_e32 v53, v53
	v_mul_f32_e32 v214, v222, v222
	v_pk_mul_f32 v[134:135], v[222:223], v[132:133] op_sel_hi:[0,1]
	v_pk_mul_f32 v[136:137], v[222:223], v[152:153] op_sel_hi:[0,1]
	v_pk_mul_f32 v[138:139], v[222:223], v[154:155] op_sel_hi:[0,1]
	v_pk_mul_f32 v[140:141], v[222:223], v[156:157] op_sel_hi:[0,1]
	v_pk_mul_f32 v[198:199], v[62:63], v[134:135]
	v_pk_mul_f32 v[200:201], v[64:65], v[136:137]
	v_pk_mul_f32 v[202:203], v[58:59], v[138:139]
	v_pk_mul_f32 v[204:205], v[60:61], v[140:141]
	v_exp_f32_e32 v198, v198
	v_exp_f32_e32 v199, v199
	v_exp_f32_e32 v200, v200
	v_exp_f32_e32 v201, v201
	v_exp_f32_e32 v202, v202
	v_exp_f32_e32 v203, v203
	v_exp_f32_e32 v204, v204
	v_exp_f32_e32 v205, v205
	v_pk_mul_f32 v[54:55], v[62:63], v[54:55]
	v_pk_mul_f32 v[56:57], v[64:65], v[56:57]
	v_pk_mul_f32 v[50:51], v[58:59], v[50:51]
	v_pk_mul_f32 v[52:53], v[60:61], v[52:53]
	v_pk_mul_f32 v[142:143], v[214:215], v[158:159] op_sel_hi:[0,1]
	v_pk_mul_f32 v[144:145], v[214:215], v[160:161] op_sel_hi:[0,1]
	v_pk_mul_f32 v[146:147], v[214:215], v[194:195] op_sel_hi:[0,1]
	v_pk_mul_f32 v[148:149], v[214:215], v[196:197] op_sel_hi:[0,1]
	v_pk_add_f32 v[198:199], v[198:199], 1.0 op_sel_hi:[1,0]
	v_pk_add_f32 v[200:201], v[200:201], 1.0 op_sel_hi:[1,0]
	v_pk_add_f32 v[202:203], v[202:203], 1.0 op_sel_hi:[1,0]
	v_pk_add_f32 v[204:205], v[204:205], 1.0 op_sel_hi:[1,0]
	v_rcp_f32_e32 v198, v198
	v_rcp_f32_e32 v199, v199
	v_rcp_f32_e32 v200, v200
	v_rcp_f32_e32 v201, v201
	v_rcp_f32_e32 v202, v202
	v_rcp_f32_e32 v203, v203
	v_rcp_f32_e32 v204, v204
	v_rcp_f32_e32 v205, v205
	v_pk_mul_f32 v[54:55], v[54:55], v[142:143]
	v_pk_mul_f32 v[56:57], v[56:57], v[144:145]
	v_pk_mul_f32 v[50:51], v[50:51], v[146:147]
	v_pk_mul_f32 v[52:53], v[52:53], v[148:149]
	s_mov_b32 s4, 0xe0000
	v_pk_mul_f32 v[54:55], v[54:55], v[198:199]
	v_pk_mul_f32 v[56:57], v[56:57], v[200:201]
	v_pk_mul_f32 v[50:51], v[50:51], v[202:203]
	v_pk_mul_f32 v[52:53], v[52:53], v[204:205]
	v_med3_f32 v54, v54, s71, v187
	v_med3_f32 v55, v55, s71, v187
	v_med3_f32 v56, v56, s71, v187
	v_med3_f32 v57, v57, s71, v187
	v_med3_f32 v50, v50, s71, v187
	v_med3_f32 v51, v51, s71, v187
	v_med3_f32 v52, v52, s71, v187
; __device__ __forceinline__ unsigned cvt4_fp8(float a, float b, float c, float d) { int w = 0; w = __builtin_amdgcn_cvt_pk_fp8_f32(clamp448(a), clamp448(b), w, false); w = __builtin_amdgcn_cvt_pk_fp8_f32(clamp448(c), clamp448(d), w, true); return (unsigned)w; }
; __device__ __forceinline__ float siluf_(float x) { return x * sigmoidf_(x); }
;     __device__ __forceinline__ void operator()(const AccT& acc, const Unit& u, int wr, int wc, int fr, int fq) const {
;     ...
;             for (int m = 0; m < 4; ++m) { const int rl = rl0 + ai * HALF + m * 16; const float rs = rs_p[rl]; f32x4 z0, z1;
;                 const i32x4v g0 = __builtin_bit_cast(i32x4v, acc[ai][0][m][0]), g1 = __builtin_bit_cast(i32x4v, acc[ai][0][m][1]), u0 = __builtin_bit_cast(i32x4v, acc[ai][1][m][0]), u1 = __builtin_bit_cast(i32x4v, acc[ai][1][m][1]);
; #pragma unroll
;                 for (int j = 0; j < 4; ++j) { z0[j] = siluf_((float)g0[j] * (rs * cg0[j])) * ((float)u0[j] * (rs * cu0[j])); z1[j] = siluf_((float)g1[j] * (rs * cg1[j])) * ((float)u1[j] * (rs * cu1[j])); }
;                 u32x2 w; w.x = cvt4_fp8(z0[0] * sout8, z0[1] * sout8, z0[2] * sout8, z0[3] * sout8); w.y = cvt4_fp8(z1[0] * sout8, z1[1] * sout8, z1[2] * sout8, z1[3] * sout8);
;                 *(u32x2*)(O + (size_t)(u.orow0 + rl) * ldo + cb) = w;
;                 __builtin_amdgcn_sched_barrier(0); }
	v_med3_f32 v53, v53, s71, v187
	v_cvt_pk_fp8_f32 v212, v54, v55
	v_cvt_pk_fp8_f32 v213, v50, v51
	v_lshl_add_u64 v[210:211], v[206:207], 0, s[4:5]
	v_cvt_pk_fp8_f32 v212, v56, v57 op_sel:[0,0,1]
	v_cvt_pk_fp8_f32 v213, v52, v53 op_sel:[0,0,1]
	s_nop 0
	global_store_dwordx2 v[210:211], v[212:213], off
	v_cvt_f32_i32_e32 v46, v46
	v_cvt_f32_i32_e32 v47, v47
	v_cvt_f32_i32_e32 v48, v48
	v_cvt_f32_i32_e32 v49, v49
	v_cvt_f32_i32_e32 v42, v42
	v_cvt_f32_i32_e32 v43, v43
	v_cvt_f32_i32_e32 v44, v44
	v_cvt_f32_i32_e32 v45, v45
	v_cvt_f32_i32_e32 v38, v38
	v_cvt_f32_i32_e32 v39, v39
	v_cvt_f32_i32_e32 v40, v40
	v_cvt_f32_i32_e32 v41, v41
	v_cvt_f32_i32_e32 v34, v34
	v_cvt_f32_i32_e32 v35, v35
	v_cvt_f32_i32_e32 v36, v36
	v_cvt_f32_i32_e32 v37, v37
	v_mul_f32_e32 v214, v223, v223
	v_pk_mul_f32 v[134:135], v[222:223], v[132:133] op_sel:[1,0] op_sel_hi:[1,1]
	v_pk_mul_f32 v[136:137], v[222:223], v[152:153] op_sel:[1,0] op_sel_hi:[1,1]
	v_pk_mul_f32 v[138:139], v[222:223], v[154:155] op_sel:[1,0] op_sel_hi:[1,1]
	v_pk_mul_f32 v[140:141], v[222:223], v[156:157] op_sel:[1,0] op_sel_hi:[1,1]
	v_pk_mul_f32 v[198:199], v[46:47], v[134:135]
	v_pk_mul_f32 v[200:201], v[48:49], v[136:137]
	v_pk_mul_f32 v[202:203], v[42:43], v[138:139]
	v_pk_mul_f32 v[204:205], v[44:45], v[140:141]
	v_exp_f32_e32 v198, v198
	v_exp_f32_e32 v199, v199
	v_exp_f32_e32 v200, v200
	v_exp_f32_e32 v201, v201
	v_exp_f32_e32 v202, v202
	v_exp_f32_e32 v203, v203
	v_exp_f32_e32 v204, v204
	v_exp_f32_e32 v205, v205
	v_pk_mul_f32 v[38:39], v[46:47], v[38:39]
	v_pk_mul_f32 v[40:41], v[48:49], v[40:41]
	v_pk_mul_f32 v[34:35], v[42:43], v[34:35]
	v_pk_mul_f32 v[36:37], v[44:45], v[36:37]
	v_pk_mul_f32 v[142:143], v[214:215], v[158:159] op_sel_hi:[0,1]
	v_pk_mul_f32 v[144:145], v[214:215], v[160:161] op_sel_hi:[0,1]
	v_pk_mul_f32 v[146:147], v[214:215], v[194:195] op_sel_hi:[0,1]
	v_pk_mul_f32 v[148:149], v[214:215], v[196:197] op_sel_hi:[0,1]
	v_pk_add_f32 v[198:199], v[198:199], 1.0 op_sel_hi:[1,0]
	v_pk_add_f32 v[200:201], v[200:201], 1.0 op_sel_hi:[1,0]
	v_pk_add_f32 v[202:203], v[202:203], 1.0 op_sel_hi:[1,0]
	v_pk_add_f32 v[204:205], v[204:205], 1.0 op_sel_hi:[1,0]
	v_rcp_f32_e32 v198, v198
	v_rcp_f32_e32 v199, v199
	v_rcp_f32_e32 v200, v200
	v_rcp_f32_e32 v201, v201
	v_rcp_f32_e32 v202, v202
	v_rcp_f32_e32 v203, v203
	v_rcp_f32_e32 v204, v204
	v_rcp_f32_e32 v205, v205
	v_pk_mul_f32 v[38:39], v[38:39], v[142:143]
	v_pk_mul_f32 v[40:41], v[40:41], v[144:145]
	v_pk_mul_f32 v[34:35], v[34:35], v[146:147]
	v_pk_mul_f32 v[36:37], v[36:37], v[148:149]
	s_mov_b32 s4, 0xfc000
	v_pk_mul_f32 v[38:39], v[38:39], v[198:199]
	v_pk_mul_f32 v[40:41], v[40:41], v[200:201]
	v_pk_mul_f32 v[34:35], v[34:35], v[202:203]
	v_pk_mul_f32 v[36:37], v[36:37], v[204:205]
	v_med3_f32 v38, v38, s71, v187
	v_med3_f32 v39, v39, s71, v187
	v_med3_f32 v40, v40, s71, v187
	v_med3_f32 v41, v41, s71, v187
	v_med3_f32 v34, v34, s71, v187
	v_med3_f32 v35, v35, s71, v187
	v_med3_f32 v36, v36, s71, v187
	v_med3_f32 v37, v37, s71, v187
	v_cvt_pk_fp8_f32 v212, v38, v39
	v_cvt_pk_fp8_f32 v213, v34, v35
	v_lshl_add_u64 v[210:211], v[206:207], 0, s[4:5]
	v_cvt_pk_fp8_f32 v212, v40, v41 op_sel:[0,0,1]
	v_cvt_pk_fp8_f32 v213, v36, v37 op_sel:[0,0,1]
	s_nop 0
	global_store_dwordx2 v[210:211], v[212:213], off
	v_cvt_f32_i32_e32 v30, v30
	v_cvt_f32_i32_e32 v31, v31
	v_cvt_f32_i32_e32 v32, v32
	v_cvt_f32_i32_e32 v33, v33
	v_cvt_f32_i32_e32 v26, v26
	v_cvt_f32_i32_e32 v27, v27
	v_cvt_f32_i32_e32 v28, v28
	v_cvt_f32_i32_e32 v29, v29
	v_cvt_f32_i32_e32 v22, v22
	v_cvt_f32_i32_e32 v23, v23
	v_cvt_f32_i32_e32 v24, v24
	v_cvt_f32_i32_e32 v25, v25
	v_cvt_f32_i32_e32 v18, v18
	v_cvt_f32_i32_e32 v19, v19
	v_cvt_f32_i32_e32 v20, v20
	v_cvt_f32_i32_e32 v21, v21
	v_mul_f32_e32 v214, v224, v224
	v_pk_mul_f32 v[134:135], v[224:225], v[132:133] op_sel_hi:[0,1]
	v_pk_mul_f32 v[136:137], v[224:225], v[152:153] op_sel_hi:[0,1]
	v_pk_mul_f32 v[138:139], v[224:225], v[154:155] op_sel_hi:[0,1]
	v_pk_mul_f32 v[140:141], v[224:225], v[156:157] op_sel_hi:[0,1]
	v_pk_mul_f32 v[198:199], v[30:31], v[134:135]
	v_pk_mul_f32 v[200:201], v[32:33], v[136:137]
	v_pk_mul_f32 v[202:203], v[26:27], v[138:139]
	v_pk_mul_f32 v[204:205], v[28:29], v[140:141]
	v_exp_f32_e32 v198, v198
	v_exp_f32_e32 v199, v199
	v_exp_f32_e32 v200, v200
	v_exp_f32_e32 v201, v201
	v_exp_f32_e32 v202, v202
	v_exp_f32_e32 v203, v203
	v_exp_f32_e32 v204, v204
	v_exp_f32_e32 v205, v205
	v_pk_mul_f32 v[22:23], v[30:31], v[22:23]
	v_pk_mul_f32 v[24:25], v[32:33], v[24:25]
	v_pk_mul_f32 v[18:19], v[26:27], v[18:19]
	v_pk_mul_f32 v[20:21], v[28:29], v[20:21]
	v_pk_mul_f32 v[142:143], v[214:215], v[158:159] op_sel_hi:[0,1]
; __device__ __forceinline__ unsigned cvt4_fp8(float a, float b, float c, float d) { int w = 0; w = __builtin_amdgcn_cvt_pk_fp8_f32(clamp448(a), clamp448(b), w, false); w = __builtin_amdgcn_cvt_pk_fp8_f32(clamp448(c), clamp448(d), w, true); return (unsigned)w; }
; __device__ __forceinline__ float siluf_(float x) { return x * sigmoidf_(x); }
;     __device__ __forceinline__ void operator()(const AccT& acc, const Unit& u, int wr, int wc, int fr, int fq) const {
;     ...
;             for (int m = 0; m < 4; ++m) { const int rl = rl0 + ai * HALF + m * 16; const float rs = rs_p[rl]; f32x4 z0, z1;
;                 const i32x4v g0 = __builtin_bit_cast(i32x4v, acc[ai][0][m][0]), g1 = __builtin_bit_cast(i32x4v, acc[ai][0][m][1]), u0 = __builtin_bit_cast(i32x4v, acc[ai][1][m][0]), u1 = __builtin_bit_cast(i32x4v, acc[ai][1][m][1]);
; #pragma unroll
;                 for (int j = 0; j < 4; ++j) { z0[j] = siluf_((float)g0[j] * (rs * cg0[j])) * ((float)u0[j] * (rs * cu0[j])); z1[j] = siluf_((float)g1[j] * (rs * cg1[j])) * ((float)u1[j] * (rs * cu1[j])); }
;                 u32x2 w; w.x = cvt4_fp8(z0[0] * sout8, z0[1] * sout8, z0[2] * sout8, z0[3] * sout8); w.y = cvt4_fp8(z1[0] * sout8, z1[1] * sout8, z1[2] * sout8, z1[3] * sout8);
;                 *(u32x2*)(O + (size_t)(u.orow0 + rl) * ldo + cb) = w;
;                 __builtin_amdgcn_sched_barrier(0); }
;     }
	v_pk_mul_f32 v[144:145], v[214:215], v[160:161] op_sel_hi:[0,1]
	v_pk_mul_f32 v[146:147], v[214:215], v[194:195] op_sel_hi:[0,1]
	v_pk_mul_f32 v[148:149], v[214:215], v[196:197] op_sel_hi:[0,1]
	v_pk_add_f32 v[198:199], v[198:199], 1.0 op_sel_hi:[1,0]
	v_pk_add_f32 v[200:201], v[200:201], 1.0 op_sel_hi:[1,0]
	v_pk_add_f32 v[202:203], v[202:203], 1.0 op_sel_hi:[1,0]
	v_pk_add_f32 v[204:205], v[204:205], 1.0 op_sel_hi:[1,0]
	v_rcp_f32_e32 v198, v198
	v_rcp_f32_e32 v199, v199
	v_rcp_f32_e32 v200, v200
	v_rcp_f32_e32 v201, v201
	v_rcp_f32_e32 v202, v202
	v_rcp_f32_e32 v203, v203
	v_rcp_f32_e32 v204, v204
	v_rcp_f32_e32 v205, v205
	v_pk_mul_f32 v[22:23], v[22:23], v[142:143]
	v_pk_mul_f32 v[24:25], v[24:25], v[144:145]
	v_pk_mul_f32 v[18:19], v[18:19], v[146:147]
	v_pk_mul_f32 v[20:21], v[20:21], v[148:149]
	s_mov_b32 s4, 0x118000
	v_pk_mul_f32 v[22:23], v[22:23], v[198:199]
	v_pk_mul_f32 v[24:25], v[24:25], v[200:201]
	v_pk_mul_f32 v[18:19], v[18:19], v[202:203]
	v_pk_mul_f32 v[20:21], v[20:21], v[204:205]
	v_med3_f32 v22, v22, s71, v187
	v_med3_f32 v23, v23, s71, v187
	v_med3_f32 v24, v24, s71, v187
	v_med3_f32 v25, v25, s71, v187
	v_med3_f32 v18, v18, s71, v187
	v_med3_f32 v19, v19, s71, v187
	v_med3_f32 v20, v20, s71, v187
	v_med3_f32 v21, v21, s71, v187
	v_cvt_pk_fp8_f32 v212, v22, v23
	v_cvt_pk_fp8_f32 v213, v18, v19
	v_lshl_add_u64 v[210:211], v[206:207], 0, s[4:5]
	v_cvt_pk_fp8_f32 v212, v24, v25 op_sel:[0,0,1]
	v_cvt_pk_fp8_f32 v213, v20, v21 op_sel:[0,0,1]
	s_nop 0
	global_store_dwordx2 v[210:211], v[212:213], off
	v_cvt_f32_i32_e32 v14, v14
	v_cvt_f32_i32_e32 v15, v15
	v_cvt_f32_i32_e32 v16, v16
	v_cvt_f32_i32_e32 v17, v17
	v_cvt_f32_i32_e32 v10, v10
	v_cvt_f32_i32_e32 v11, v11
	v_cvt_f32_i32_e32 v12, v12
	v_cvt_f32_i32_e32 v13, v13
	v_cvt_f32_i32_e32 v6, v6
	v_cvt_f32_i32_e32 v7, v7
	v_cvt_f32_i32_e32 v8, v8
	v_cvt_f32_i32_e32 v9, v9
	v_cvt_f32_i32_e32 v2, v2
	v_cvt_f32_i32_e32 v3, v3
	v_cvt_f32_i32_e32 v4, v4
	v_cvt_f32_i32_e32 v5, v5
	v_mul_f32_e32 v214, v225, v225
	v_pk_mul_f32 v[134:135], v[224:225], v[132:133] op_sel:[1,0] op_sel_hi:[1,1]
	v_pk_mul_f32 v[136:137], v[224:225], v[152:153] op_sel:[1,0] op_sel_hi:[1,1]
	v_pk_mul_f32 v[138:139], v[224:225], v[154:155] op_sel:[1,0] op_sel_hi:[1,1]
	v_pk_mul_f32 v[140:141], v[224:225], v[156:157] op_sel:[1,0] op_sel_hi:[1,1]
	v_pk_mul_f32 v[198:199], v[14:15], v[134:135]
	v_pk_mul_f32 v[200:201], v[16:17], v[136:137]
	v_pk_mul_f32 v[202:203], v[10:11], v[138:139]
	v_pk_mul_f32 v[204:205], v[12:13], v[140:141]
	v_exp_f32_e32 v198, v198
	v_exp_f32_e32 v199, v199
	v_exp_f32_e32 v200, v200
	v_exp_f32_e32 v201, v201
	v_exp_f32_e32 v202, v202
	v_exp_f32_e32 v203, v203
	v_exp_f32_e32 v204, v204
	v_exp_f32_e32 v205, v205
	v_pk_mul_f32 v[6:7], v[14:15], v[6:7]
	v_pk_mul_f32 v[8:9], v[16:17], v[8:9]
	v_pk_mul_f32 v[2:3], v[10:11], v[2:3]
	v_pk_mul_f32 v[4:5], v[12:13], v[4:5]
	v_pk_mul_f32 v[142:143], v[214:215], v[158:159] op_sel_hi:[0,1]
	v_pk_mul_f32 v[144:145], v[214:215], v[160:161] op_sel_hi:[0,1]
	v_pk_mul_f32 v[146:147], v[214:215], v[194:195] op_sel_hi:[0,1]
	v_pk_mul_f32 v[148:149], v[214:215], v[196:197] op_sel_hi:[0,1]
	v_pk_add_f32 v[198:199], v[198:199], 1.0 op_sel_hi:[1,0]
	v_pk_add_f32 v[200:201], v[200:201], 1.0 op_sel_hi:[1,0]
	v_pk_add_f32 v[202:203], v[202:203], 1.0 op_sel_hi:[1,0]
	v_pk_add_f32 v[204:205], v[204:205], 1.0 op_sel_hi:[1,0]
	v_rcp_f32_e32 v198, v198
	v_rcp_f32_e32 v199, v199
	v_rcp_f32_e32 v200, v200
	v_rcp_f32_e32 v201, v201
	v_rcp_f32_e32 v202, v202
	v_rcp_f32_e32 v203, v203
	v_rcp_f32_e32 v204, v204
	v_rcp_f32_e32 v205, v205
	v_pk_mul_f32 v[6:7], v[6:7], v[142:143]
	v_pk_mul_f32 v[8:9], v[8:9], v[144:145]
	v_pk_mul_f32 v[2:3], v[2:3], v[146:147]
	v_pk_mul_f32 v[4:5], v[4:5], v[148:149]
	s_mov_b32 s4, 0x134000
	v_pk_mul_f32 v[6:7], v[6:7], v[198:199]
	v_pk_mul_f32 v[8:9], v[8:9], v[200:201]
	v_pk_mul_f32 v[2:3], v[2:3], v[202:203]
	v_pk_mul_f32 v[4:5], v[4:5], v[204:205]
	v_med3_f32 v6, v6, s71, v187
	v_med3_f32 v7, v7, s71, v187
	v_med3_f32 v8, v8, s71, v187
	v_med3_f32 v9, v9, s71, v187
	v_med3_f32 v2, v2, s71, v187
	v_med3_f32 v3, v3, s71, v187
	v_med3_f32 v4, v4, s71, v187
	v_med3_f32 v5, v5, s71, v187
	v_cvt_pk_fp8_f32 v212, v6, v7
	v_cvt_pk_fp8_f32 v213, v2, v3
	v_lshl_add_u64 v[210:211], v[206:207], 0, s[4:5]
	v_cvt_pk_fp8_f32 v212, v8, v9 op_sel:[0,0,1]
	v_cvt_pk_fp8_f32 v213, v4, v5 op_sel:[0,0,1]
	s_nop 0
	global_store_dwordx2 v[210:211], v[212:213], off
	s_and_b64 vcc, exec, s[2:3]
	s_mov_b64 s[2:3], -1
	s_cbranch_vccnz .LBB0_2537
	s_andn2_b64 vcc, exec, s[18:19]
	s_cbranch_vccnz .LBB0_2536
	s_barrier
	s_branch .LBB0_2536

; __global__ void __launch_bounds__(512, 2) fwd_kernel(Params KP) {
	.amdhsa_kernel _Z10fwd_kernel6Params
		.amdhsa_group_segment_fixed_size 0
		.amdhsa_private_segment_fixed_size 0
		.amdhsa_kernarg_size 312
		.amdhsa_user_sgpr_count 2
		.amdhsa_user_sgpr_dispatch_ptr 0
		.amdhsa_user_sgpr_queue_ptr 0
		.amdhsa_user_sgpr_kernarg_segment_ptr 1
		.amdhsa_user_sgpr_dispatch_id 0
		.amdhsa_user_sgpr_kernarg_preload_length 0
		.amdhsa_user_sgpr_kernarg_preload_offset 0
		.amdhsa_user_sgpr_private_segment_size 0
		.amdhsa_uses_dynamic_stack 0
		.amdhsa_enable_private_segment 0
		.amdhsa_system_sgpr_workgroup_id_x 1
		.amdhsa_system_sgpr_workgroup_id_y 0
		.amdhsa_system_sgpr_workgroup_id_z 0
		.amdhsa_system_sgpr_workgroup_info 0
		.amdhsa_system_vgpr_workitem_id 0
		.amdhsa_next_free_vgpr 252
		.amdhsa_next_free_sgpr 102
		.amdhsa_accum_offset 252
		.amdhsa_reserve_vcc 1
		.amdhsa_float_round_mode_32 0
		.amdhsa_float_round_mode_16_64 0
		.amdhsa_float_denorm_mode_32 3
		.amdhsa_float_denorm_mode_16_64 3
		.amdhsa_dx10_clamp 1
		.amdhsa_ieee_mode 1
		.amdhsa_fp16_overflow 0
		.amdhsa_tg_split 0
		.amdhsa_exception_fp_ieee_invalid_op 0
		.amdhsa_exception_fp_denorm_src 0
		.amdhsa_exception_fp_ieee_div_zero 0
		.amdhsa_exception_fp_ieee_overflow 0
		.amdhsa_exception_fp_ieee_underflow 0
		.amdhsa_exception_fp_ieee_inexact 0
		.amdhsa_exception_int_div_zero 0
	.end_amdhsa_kernel

; __global__ void __launch_bounds__(512, 2) fwd_kernel(Params KP) {
amdhsa.kernels:
  - .agpr_count:     0
    .args:
      - .offset:         0
        .size:           312
        .value_kind:     by_value
    .group_segment_fixed_size: 0
    .kernarg_segment_align: 8
    .kernarg_segment_size: 312
    .language:       OpenCL C
    .language_version:
      - 2
      - 0
    .max_flat_workgroup_size: 512
    .name:           _Z10fwd_kernel6Params
    .private_segment_fixed_size: 0
    .sgpr_count:     108
    .sgpr_spill_count: 0
    .symbol:         _Z10fwd_kernel6Params.kd
    .uniform_work_group_size: 1
    .uses_dynamic_stack: false
    .vgpr_count:     252
    .vgpr_spill_count: 0
    .wavefront_size: 64
